# expert-table conversion loops (U and V) software-pipelined one row ahead with counted vmcnt leaving stores outstanding
# baseline (speedup 1.0000x reference)
; __device__ __forceinline__ unsigned q4(float x) { return (unsigned)(int)fminf(fmaxf(rintf(x), -7.0f), 7.0f) & 0xfu; }
; __device__ __forceinline__ void cvt_table_i4(const float* src, unsigned char* dst, float* scl, float scl_mul, int gw, int ngw, int lane) {
;     for (int row = gw; row < 16384; row += ngw) {
;         const f32x4* sp = (const f32x4*)(src + (size_t)row * 1024 + 16 * lane);
;         const f32x4 a0 = sp[0], a1 = sp[1], a2 = sp[2], a3 = sp[3];
;         float ss = ((a0.x * a0.x + a0.y * a0.y) + (a0.z * a0.z + a0.w * a0.w)) + ((a1.x * a1.x + a1.y * a1.y) + (a1.z * a1.z + a1.w * a1.w))
;                  + ((a2.x * a2.x + a2.y * a2.y) + (a2.z * a2.z + a2.w * a2.w)) + ((a3.x * a3.x + a3.y * a3.y) + (a3.z * a3.z + a3.w * a3.w));
;         ss = wave_sum(ss);
;         const float step = fmaxf(0.35f * sqrtf(ss * (1.0f / 1024.0f)), 1e-30f), q = 1.0f / step;
;         v2u o;
;         o.x = (q4(a0.x * q) | (q4(a1.x * q) << 4)) | ((q4(a0.y * q) | (q4(a1.y * q) << 4)) << 8) | ((q4(a0.z * q) | (q4(a1.z * q) << 4)) << 16) | ((q4(a0.w * q) | (q4(a1.w * q) << 4)) << 24);
;         o.y = (q4(a2.x * q) | (q4(a3.x * q) << 4)) | ((q4(a2.y * q) | (q4(a3.y * q) << 4)) << 8) | ((q4(a2.z * q) | (q4(a3.z * q) << 4)) << 16) | ((q4(a2.w * q) | (q4(a3.w * q) << 4)) << 24);
;         *(v2u*)(dst + (size_t)row * 512 + 8 * lane) = o;
;         if (lane == 0) scl[row] = step * scl_mul;
;     }
.LBB0_1973:
	global_load_dwordx4 v[8:11], v[4:5], off offset:-32
	global_load_dwordx4 v[12:15], v[4:5], off offset:-16
	global_load_dwordx4 v[20:23], v[4:5], off
	global_load_dwordx4 v[24:27], v[4:5], off offset:16
	s_add_i32 s15, s15, s18
	v_lshl_add_u64 v[4:5], v[4:5], 0, s[46:47]
	s_cmpk_lt_i32 s15, 0x4000
	s_cbranch_scc0 .Ltabv_lastA0
	global_load_dwordx4 v[48:51], v[4:5], off offset:-32
	global_load_dwordx4 v[52:55], v[4:5], off offset:-16
	global_load_dwordx4 v[60:63], v[4:5], off
	global_load_dwordx4 v[64:67], v[4:5], off offset:16
	s_waitcnt vmcnt(4)
	v_mul_f32_e32 v7, v9, v9
	v_mul_f32_e32 v16, v11, v11
	v_mul_f32_e32 v17, v13, v13
	v_mul_f32_e32 v28, v15, v15
	v_mul_f32_e32 v29, v21, v21
	v_mul_f32_e32 v30, v23, v23
	v_fmac_f32_e32 v7, v8, v8
	v_fmac_f32_e32 v16, v10, v10
	v_fmac_f32_e32 v17, v12, v12
	v_fmac_f32_e32 v28, v14, v14
	v_mul_f32_e32 v31, v25, v25
	v_mul_f32_e32 v32, v27, v27
	v_fmac_f32_e32 v29, v20, v20
	v_fmac_f32_e32 v30, v22, v22
	v_add_f32_e32 v7, v7, v16
	v_add_f32_e32 v16, v17, v28
	v_fmac_f32_e32 v31, v24, v24
	v_fmac_f32_e32 v32, v26, v26
	v_add_f32_e32 v17, v29, v30
	v_add_f32_e32 v7, v7, v16
	v_add_f32_e32 v28, v31, v32
	v_add_f32_e32 v7, v7, v17
	v_add_f32_e32 v7, v7, v28
	s_nop 1
	v_add_f32_dpp v7, v7, v7 quad_perm:[1,0,3,2] row_mask:0xf bank_mask:0xf bound_ctrl:1
	s_nop 1
	v_add_f32_dpp v7, v7, v7 quad_perm:[2,3,0,1] row_mask:0xf bank_mask:0xf bound_ctrl:1
	s_nop 1
	v_add_f32_dpp v7, v7, v7 row_half_mirror row_mask:0xf bank_mask:0xf bound_ctrl:1
	s_nop 1
	v_add_f32_dpp v7, v7, v7 row_mirror row_mask:0xf bank_mask:0xf bound_ctrl:1
	v_mov_b32_e32 v16, v7
	s_nop 1
	v_permlane16_swap_b32_e32 v7, v16
	v_add_f32 v7, v7, v16
	s_nop 1
	s_nop 0
	v_mov_b32_e32 v16, v7
	s_nop 1
	v_permlane32_swap_b32_e32 v7, v16
	v_add_f32 v7, v7, v16
	s_nop 0
	v_mul_f32_e32 v7, 0x3a800000, v7
	v_mul_f32_e32 v16, 0x4f800000, v7
	v_cmp_gt_f32_e32 vcc, s3, v7
	s_nop 1
	v_cndmask_b32_e32 v7, v7, v16, vcc
	v_sqrt_f32_e32 v16, v7
	s_nop 0
	v_add_u32_e32 v17, -1, v16
	v_add_u32_e32 v28, 1, v16
	v_fma_f32 v29, -v17, v16, v7
	v_fma_f32 v30, -v28, v16, v7
	v_cmp_ge_f32_e64 s[0:1], 0, v29
	s_nop 1
	v_cndmask_b32_e64 v16, v16, v17, s[0:1]
	v_cmp_lt_f32_e64 s[0:1], 0, v30
	s_nop 1
	v_cndmask_b32_e64 v16, v16, v28, s[0:1]
	v_mul_f32_e32 v17, 0x37800000, v16
	v_cndmask_b32_e32 v16, v16, v17, vcc
	v_cmp_class_f32_e32 vcc, v7, v1
	s_nop 1
	v_cndmask_b32_e32 v7, v16, v7, vcc
	v_mul_f32_e32 v7, 0x3eb33333, v7
	v_max_f32_e32 v7, 0xda24260, v7
	v_div_scale_f32 v16, s[0:1], v7, v7, 1.0
	v_rcp_f32_e32 v17, v16
	v_div_scale_f32 v28, vcc, 1.0, v7, 1.0
	v_fma_f32 v29, -v16, v17, 1.0
	v_fmac_f32_e32 v17, v29, v17
	v_mul_f32_e32 v29, v28, v17
	v_fma_f32 v30, -v16, v29, v28
	v_fmac_f32_e32 v29, v30, v17
	v_fma_f32 v16, -v16, v29, v28
	v_div_fmas_f32 v16, v16, v17, v29
	v_div_fixup_f32 v16, v16, v7, 1.0
	v_mul_f32_e32 v8, v8, v16
	v_mul_f32_e32 v9, v9, v16
	v_mul_f32_e32 v10, v10, v16
	v_mul_f32_e32 v11, v11, v16
	v_mul_f32_e32 v12, v12, v16
	v_mul_f32_e32 v13, v13, v16
	v_mul_f32_e32 v14, v14, v16
	v_mul_f32_e32 v15, v15, v16
	v_mul_f32_e32 v20, v20, v16
	v_mul_f32_e32 v21, v21, v16
	v_mul_f32_e32 v22, v22, v16
	v_mul_f32_e32 v23, v23, v16
	v_mul_f32_e32 v24, v24, v16
	v_mul_f32_e32 v25, v25, v16
	v_mul_f32_e32 v26, v26, v16
	v_mul_f32_e32 v27, v27, v16
	v_rndne_f32_e32 v8, v8
	v_rndne_f32_e32 v9, v9
	v_rndne_f32_e32 v10, v10
	v_rndne_f32_e32 v11, v11
	v_rndne_f32_e32 v12, v12
	v_rndne_f32_e32 v13, v13
	v_rndne_f32_e32 v14, v14
	v_rndne_f32_e32 v15, v15
	v_rndne_f32_e32 v20, v20
	v_rndne_f32_e32 v21, v21
	v_rndne_f32_e32 v22, v22
	v_rndne_f32_e32 v23, v23
	v_rndne_f32_e32 v24, v24
	v_rndne_f32_e32 v25, v25
	v_rndne_f32_e32 v26, v26
	v_rndne_f32_e32 v27, v27
	v_med3_f32 v8, v8, s13, v6
	v_med3_f32 v9, v9, s13, v6
	v_med3_f32 v10, v10, s13, v6
	v_med3_f32 v11, v11, s13, v6
	v_med3_f32 v12, v12, s13, v6
	v_med3_f32 v13, v13, s13, v6
	v_med3_f32 v14, v14, s13, v6
	v_med3_f32 v15, v15, s13, v6
	v_med3_f32 v20, v20, s13, v6
	v_med3_f32 v21, v21, s13, v6
	v_med3_f32 v22, v22, s13, v6
	v_med3_f32 v23, v23, s13, v6
	v_med3_f32 v24, v24, s13, v6
	v_med3_f32 v25, v25, s13, v6
	v_med3_f32 v26, v26, s13, v6
	v_med3_f32 v27, v27, s13, v6
	v_fmamk_f32 v8, v12, 0x41800000, v8
	v_fmamk_f32 v20, v24, 0x41800000, v20
	v_fmamk_f32 v9, v13, 0x41800000, v9
	v_fmamk_f32 v21, v25, 0x41800000, v21
	v_fmamk_f32 v10, v14, 0x41800000, v10
	v_fmamk_f32 v22, v26, 0x41800000, v22
	v_fmamk_f32 v11, v15, 0x41800000, v11
	v_fmamk_f32 v23, v27, 0x41800000, v23
	v_add_f32_e32 v8, 0x41000000, v8
	v_add_f32_e32 v20, 0x41000000, v20
	v_add_f32_e32 v9, 0x41000000, v9
	v_add_f32_e32 v21, 0x41000000, v21
	v_add_f32_e32 v10, 0x41000000, v10
	v_add_f32_e32 v22, 0x41000000, v22
	v_add_f32_e32 v11, 0x41000000, v11
	v_add_f32_e32 v23, 0x41000000, v23
	v_cvt_i32_f32_e32 v12, v8
	v_cvt_i32_f32_e32 v13, v20
	v_cvt_i32_f32_sdwa v12, v9 dst_sel:BYTE_1 dst_unused:UNUSED_PRESERVE src0_sel:DWORD
	v_cvt_i32_f32_sdwa v13, v21 dst_sel:BYTE_1 dst_unused:UNUSED_PRESERVE src0_sel:DWORD
	v_cvt_i32_f32_sdwa v12, v10 dst_sel:BYTE_2 dst_unused:UNUSED_PRESERVE src0_sel:DWORD
	v_cvt_i32_f32_sdwa v13, v22 dst_sel:BYTE_2 dst_unused:UNUSED_PRESERVE src0_sel:DWORD
	v_cvt_i32_f32_sdwa v12, v11 dst_sel:BYTE_3 dst_unused:UNUSED_PRESERVE src0_sel:DWORD
	v_cvt_i32_f32_sdwa v13, v23 dst_sel:BYTE_3 dst_unused:UNUSED_PRESERVE src0_sel:DWORD
	s_nop 0
	global_store_dwordx2 v[2:3], v[12:13], off
	s_and_saveexec_b64 s[0:1], s[4:5]
	v_mul_f32_e32 v7, 0x3d800000, v7
	global_store_dword v19, v7, s[6:7]
	s_or_b64 exec, exec, s[0:1]
	s_add_u32 s6, s6, s42
	s_addc_u32 s7, s7, s43
	v_lshl_add_u64 v[2:3], v[2:3], 0, s[44:45]
; __device__ __forceinline__ unsigned q4(float x) { return (unsigned)(int)fminf(fmaxf(rintf(x), -7.0f), 7.0f) & 0xfu; }
; __device__ __forceinline__ void cvt_table_i4(const float* src, unsigned char* dst, float* scl, float scl_mul, int gw, int ngw, int lane) {
;     for (int row = gw; row < 16384; row += ngw) {
;         const f32x4* sp = (const f32x4*)(src + (size_t)row * 1024 + 16 * lane);
;         const f32x4 a0 = sp[0], a1 = sp[1], a2 = sp[2], a3 = sp[3];
;         float ss = ((a0.x * a0.x + a0.y * a0.y) + (a0.z * a0.z + a0.w * a0.w)) + ((a1.x * a1.x + a1.y * a1.y) + (a1.z * a1.z + a1.w * a1.w))
;                  + ((a2.x * a2.x + a2.y * a2.y) + (a2.z * a2.z + a2.w * a2.w)) + ((a3.x * a3.x + a3.y * a3.y) + (a3.z * a3.z + a3.w * a3.w));
;         ss = wave_sum(ss);
;         const float step = fmaxf(0.35f * sqrtf(ss * (1.0f / 1024.0f)), 1e-30f), q = 1.0f / step;
;         v2u o;
;         o.x = (q4(a0.x * q) | (q4(a1.x * q) << 4)) | ((q4(a0.y * q) | (q4(a1.y * q) << 4)) << 8) | ((q4(a0.z * q) | (q4(a1.z * q) << 4)) << 16) | ((q4(a0.w * q) | (q4(a1.w * q) << 4)) << 24);
;         o.y = (q4(a2.x * q) | (q4(a3.x * q) << 4)) | ((q4(a2.y * q) | (q4(a3.y * q) << 4)) << 8) | ((q4(a2.z * q) | (q4(a3.z * q) << 4)) << 16) | ((q4(a2.w * q) | (q4(a3.w * q) << 4)) << 24);
;         *(v2u*)(dst + (size_t)row * 512 + 8 * lane) = o;
;         if (lane == 0) scl[row] = step * scl_mul;
;     }
.Ltabv_loop:
	s_add_i32 s15, s15, s18
	v_lshl_add_u64 v[4:5], v[4:5], 0, s[46:47]
	s_cmpk_lt_i32 s15, 0x4000
	s_cbranch_scc0 .Ltabv_lastB
	global_load_dwordx4 v[8:11], v[4:5], off offset:-32
	global_load_dwordx4 v[12:15], v[4:5], off offset:-16
	global_load_dwordx4 v[20:23], v[4:5], off
	global_load_dwordx4 v[24:27], v[4:5], off offset:16
	s_waitcnt vmcnt(6)
	v_mul_f32_e32 v47, v49, v49
	v_mul_f32_e32 v56, v51, v51
	v_mul_f32_e32 v57, v53, v53
	v_mul_f32_e32 v68, v55, v55
	v_mul_f32_e32 v69, v61, v61
	v_mul_f32_e32 v70, v63, v63
	v_fmac_f32_e32 v47, v48, v48
	v_fmac_f32_e32 v56, v50, v50
	v_fmac_f32_e32 v57, v52, v52
	v_fmac_f32_e32 v68, v54, v54
	v_mul_f32_e32 v71, v65, v65
	v_mul_f32_e32 v72, v67, v67
	v_fmac_f32_e32 v69, v60, v60
	v_fmac_f32_e32 v70, v62, v62
	v_add_f32_e32 v47, v47, v56
	v_add_f32_e32 v56, v57, v68
	v_fmac_f32_e32 v71, v64, v64
	v_fmac_f32_e32 v72, v66, v66
	v_add_f32_e32 v57, v69, v70
	v_add_f32_e32 v47, v47, v56
	v_add_f32_e32 v68, v71, v72
	v_add_f32_e32 v47, v47, v57
	v_add_f32_e32 v47, v47, v68
	s_nop 1
	v_add_f32_dpp v47, v47, v47 quad_perm:[1,0,3,2] row_mask:0xf bank_mask:0xf bound_ctrl:1
	s_nop 1
	v_add_f32_dpp v47, v47, v47 quad_perm:[2,3,0,1] row_mask:0xf bank_mask:0xf bound_ctrl:1
	s_nop 1
	v_add_f32_dpp v47, v47, v47 row_half_mirror row_mask:0xf bank_mask:0xf bound_ctrl:1
	s_nop 1
	v_add_f32_dpp v47, v47, v47 row_mirror row_mask:0xf bank_mask:0xf bound_ctrl:1
	v_mov_b32_e32 v56, v47
	s_nop 1
	v_permlane16_swap_b32_e32 v47, v56
	v_add_f32 v47, v47, v56
	s_nop 1
	s_nop 0
	v_mov_b32_e32 v56, v47
	s_nop 1
	v_permlane32_swap_b32_e32 v47, v56
	v_add_f32 v47, v47, v56
	s_nop 0
	v_mul_f32_e32 v47, 0x3a800000, v47
	v_mul_f32_e32 v56, 0x4f800000, v47
	v_cmp_gt_f32_e32 vcc, s3, v47
	s_nop 1
	v_cndmask_b32_e32 v47, v47, v56, vcc
	v_sqrt_f32_e32 v56, v47
	s_nop 0
	v_add_u32_e32 v57, -1, v56
	v_add_u32_e32 v68, 1, v56
	v_fma_f32 v69, -v57, v56, v47
	v_fma_f32 v70, -v68, v56, v47
	v_cmp_ge_f32_e64 s[0:1], 0, v69
	s_nop 1
	v_cndmask_b32_e64 v56, v56, v57, s[0:1]
	v_cmp_lt_f32_e64 s[0:1], 0, v70
	s_nop 1
	v_cndmask_b32_e64 v56, v56, v68, s[0:1]
	v_mul_f32_e32 v57, 0x37800000, v56
	v_cndmask_b32_e32 v56, v56, v57, vcc
	v_cmp_class_f32_e32 vcc, v47, v1
	s_nop 1
	v_cndmask_b32_e32 v47, v56, v47, vcc
	v_mul_f32_e32 v47, 0x3eb33333, v47
	v_max_f32_e32 v47, 0xda24260, v47
	v_div_scale_f32 v56, s[0:1], v47, v47, 1.0
	v_rcp_f32_e32 v57, v56
	v_div_scale_f32 v68, vcc, 1.0, v47, 1.0
	v_fma_f32 v69, -v56, v57, 1.0
	v_fmac_f32_e32 v57, v69, v57
	v_mul_f32_e32 v69, v68, v57
	v_fma_f32 v70, -v56, v69, v68
	v_fmac_f32_e32 v69, v70, v57
	v_fma_f32 v56, -v56, v69, v68
	v_div_fmas_f32 v56, v56, v57, v69
	v_div_fixup_f32 v56, v56, v47, 1.0
	v_mul_f32_e32 v48, v48, v56
	v_mul_f32_e32 v49, v49, v56
	v_mul_f32_e32 v50, v50, v56
	v_mul_f32_e32 v51, v51, v56
	v_mul_f32_e32 v52, v52, v56
	v_mul_f32_e32 v53, v53, v56
	v_mul_f32_e32 v54, v54, v56
	v_mul_f32_e32 v55, v55, v56
	v_mul_f32_e32 v60, v60, v56
	v_mul_f32_e32 v61, v61, v56
	v_mul_f32_e32 v62, v62, v56
	v_mul_f32_e32 v63, v63, v56
	v_mul_f32_e32 v64, v64, v56
	v_mul_f32_e32 v65, v65, v56
	v_mul_f32_e32 v66, v66, v56
	v_mul_f32_e32 v67, v67, v56
	v_rndne_f32_e32 v48, v48
	v_rndne_f32_e32 v49, v49
	v_rndne_f32_e32 v50, v50
	v_rndne_f32_e32 v51, v51
	v_rndne_f32_e32 v52, v52
	v_rndne_f32_e32 v53, v53
	v_rndne_f32_e32 v54, v54
	v_rndne_f32_e32 v55, v55
	v_rndne_f32_e32 v60, v60
	v_rndne_f32_e32 v61, v61
	v_rndne_f32_e32 v62, v62
	v_rndne_f32_e32 v63, v63
	v_rndne_f32_e32 v64, v64
	v_rndne_f32_e32 v65, v65
	v_rndne_f32_e32 v66, v66
	v_rndne_f32_e32 v67, v67
	v_med3_f32 v48, v48, s13, v6
	v_med3_f32 v49, v49, s13, v6
	v_med3_f32 v50, v50, s13, v6
	v_med3_f32 v51, v51, s13, v6
	v_med3_f32 v52, v52, s13, v6
	v_med3_f32 v53, v53, s13, v6
	v_med3_f32 v54, v54, s13, v6
	v_med3_f32 v55, v55, s13, v6
	v_med3_f32 v60, v60, s13, v6
	v_med3_f32 v61, v61, s13, v6
	v_med3_f32 v62, v62, s13, v6
	v_med3_f32 v63, v63, s13, v6
	v_med3_f32 v64, v64, s13, v6
	v_med3_f32 v65, v65, s13, v6
	v_med3_f32 v66, v66, s13, v6
	v_med3_f32 v67, v67, s13, v6
	v_fmamk_f32 v48, v52, 0x41800000, v48
	v_fmamk_f32 v60, v64, 0x41800000, v60
	v_fmamk_f32 v49, v53, 0x41800000, v49
	v_fmamk_f32 v61, v65, 0x41800000, v61
	v_fmamk_f32 v50, v54, 0x41800000, v50
	v_fmamk_f32 v62, v66, 0x41800000, v62
	v_fmamk_f32 v51, v55, 0x41800000, v51
	v_fmamk_f32 v63, v67, 0x41800000, v63
	v_add_f32_e32 v48, 0x41000000, v48
	v_add_f32_e32 v60, 0x41000000, v60
	v_add_f32_e32 v49, 0x41000000, v49
	v_add_f32_e32 v61, 0x41000000, v61
	v_add_f32_e32 v50, 0x41000000, v50
	v_add_f32_e32 v62, 0x41000000, v62
	v_add_f32_e32 v51, 0x41000000, v51
	v_add_f32_e32 v63, 0x41000000, v63
	v_cvt_i32_f32_e32 v52, v48
	v_cvt_i32_f32_e32 v53, v60
	v_cvt_i32_f32_sdwa v52, v49 dst_sel:BYTE_1 dst_unused:UNUSED_PRESERVE src0_sel:DWORD
	v_cvt_i32_f32_sdwa v53, v61 dst_sel:BYTE_1 dst_unused:UNUSED_PRESERVE src0_sel:DWORD
	v_cvt_i32_f32_sdwa v52, v50 dst_sel:BYTE_2 dst_unused:UNUSED_PRESERVE src0_sel:DWORD
	v_cvt_i32_f32_sdwa v53, v62 dst_sel:BYTE_2 dst_unused:UNUSED_PRESERVE src0_sel:DWORD
	v_cvt_i32_f32_sdwa v52, v51 dst_sel:BYTE_3 dst_unused:UNUSED_PRESERVE src0_sel:DWORD
	v_cvt_i32_f32_sdwa v53, v63 dst_sel:BYTE_3 dst_unused:UNUSED_PRESERVE src0_sel:DWORD
	s_nop 0
	global_store_dwordx2 v[2:3], v[52:53], off
	s_and_saveexec_b64 s[0:1], s[4:5]
	v_mul_f32_e32 v47, 0x3d800000, v47
	global_store_dword v19, v47, s[6:7]
	s_or_b64 exec, exec, s[0:1]
	s_add_u32 s6, s6, s42
	s_addc_u32 s7, s7, s43
	v_lshl_add_u64 v[2:3], v[2:3], 0, s[44:45]
	s_add_i32 s15, s15, s18
	v_lshl_add_u64 v[4:5], v[4:5], 0, s[46:47]
	s_cmpk_lt_i32 s15, 0x4000
	s_cbranch_scc0 .Ltabv_lastA
; __device__ __forceinline__ unsigned q4(float x) { return (unsigned)(int)fminf(fmaxf(rintf(x), -7.0f), 7.0f) & 0xfu; }
; __device__ __forceinline__ void cvt_table_i4(const float* src, unsigned char* dst, float* scl, float scl_mul, int gw, int ngw, int lane) {
;     for (int row = gw; row < 16384; row += ngw) {
;         const f32x4* sp = (const f32x4*)(src + (size_t)row * 1024 + 16 * lane);
;         const f32x4 a0 = sp[0], a1 = sp[1], a2 = sp[2], a3 = sp[3];
;         float ss = ((a0.x * a0.x + a0.y * a0.y) + (a0.z * a0.z + a0.w * a0.w)) + ((a1.x * a1.x + a1.y * a1.y) + (a1.z * a1.z + a1.w * a1.w))
;                  + ((a2.x * a2.x + a2.y * a2.y) + (a2.z * a2.z + a2.w * a2.w)) + ((a3.x * a3.x + a3.y * a3.y) + (a3.z * a3.z + a3.w * a3.w));
;         ss = wave_sum(ss);
;         const float step = fmaxf(0.35f * sqrtf(ss * (1.0f / 1024.0f)), 1e-30f), q = 1.0f / step;
;         v2u o;
;         o.x = (q4(a0.x * q) | (q4(a1.x * q) << 4)) | ((q4(a0.y * q) | (q4(a1.y * q) << 4)) << 8) | ((q4(a0.z * q) | (q4(a1.z * q) << 4)) << 16) | ((q4(a0.w * q) | (q4(a1.w * q) << 4)) << 24);
;         o.y = (q4(a2.x * q) | (q4(a3.x * q) << 4)) | ((q4(a2.y * q) | (q4(a3.y * q) << 4)) << 8) | ((q4(a2.z * q) | (q4(a3.z * q) << 4)) << 16) | ((q4(a2.w * q) | (q4(a3.w * q) << 4)) << 24);
;         *(v2u*)(dst + (size_t)row * 512 + 8 * lane) = o;
;         if (lane == 0) scl[row] = step * scl_mul;
;     }
	global_load_dwordx4 v[48:51], v[4:5], off offset:-32
	global_load_dwordx4 v[52:55], v[4:5], off offset:-16
	global_load_dwordx4 v[60:63], v[4:5], off
	global_load_dwordx4 v[64:67], v[4:5], off offset:16
	s_waitcnt vmcnt(6)
	v_mul_f32_e32 v7, v9, v9
	v_mul_f32_e32 v16, v11, v11
	v_mul_f32_e32 v17, v13, v13
	v_mul_f32_e32 v28, v15, v15
	v_mul_f32_e32 v29, v21, v21
	v_mul_f32_e32 v30, v23, v23
	v_fmac_f32_e32 v7, v8, v8
	v_fmac_f32_e32 v16, v10, v10
	v_fmac_f32_e32 v17, v12, v12
	v_fmac_f32_e32 v28, v14, v14
	v_mul_f32_e32 v31, v25, v25
	v_mul_f32_e32 v32, v27, v27
	v_fmac_f32_e32 v29, v20, v20
	v_fmac_f32_e32 v30, v22, v22
	v_add_f32_e32 v7, v7, v16
	v_add_f32_e32 v16, v17, v28
	v_fmac_f32_e32 v31, v24, v24
	v_fmac_f32_e32 v32, v26, v26
	v_add_f32_e32 v17, v29, v30
	v_add_f32_e32 v7, v7, v16
	v_add_f32_e32 v28, v31, v32
	v_add_f32_e32 v7, v7, v17
	v_add_f32_e32 v7, v7, v28
	s_nop 1
	v_add_f32_dpp v7, v7, v7 quad_perm:[1,0,3,2] row_mask:0xf bank_mask:0xf bound_ctrl:1
	s_nop 1
	v_add_f32_dpp v7, v7, v7 quad_perm:[2,3,0,1] row_mask:0xf bank_mask:0xf bound_ctrl:1
	s_nop 1
	v_add_f32_dpp v7, v7, v7 row_half_mirror row_mask:0xf bank_mask:0xf bound_ctrl:1
	s_nop 1
	v_add_f32_dpp v7, v7, v7 row_mirror row_mask:0xf bank_mask:0xf bound_ctrl:1
	v_mov_b32_e32 v16, v7
	s_nop 1
	v_permlane16_swap_b32_e32 v7, v16
	v_add_f32 v7, v7, v16
	s_nop 1
	s_nop 0
	v_mov_b32_e32 v16, v7
	s_nop 1
	v_permlane32_swap_b32_e32 v7, v16
	v_add_f32 v7, v7, v16
	s_nop 0
	v_mul_f32_e32 v7, 0x3a800000, v7
	v_mul_f32_e32 v16, 0x4f800000, v7
	v_cmp_gt_f32_e32 vcc, s3, v7
	s_nop 1
	v_cndmask_b32_e32 v7, v7, v16, vcc
	v_sqrt_f32_e32 v16, v7
	s_nop 0
	v_add_u32_e32 v17, -1, v16
	v_add_u32_e32 v28, 1, v16
	v_fma_f32 v29, -v17, v16, v7
	v_fma_f32 v30, -v28, v16, v7
	v_cmp_ge_f32_e64 s[0:1], 0, v29
	s_nop 1
	v_cndmask_b32_e64 v16, v16, v17, s[0:1]
	v_cmp_lt_f32_e64 s[0:1], 0, v30
	s_nop 1
	v_cndmask_b32_e64 v16, v16, v28, s[0:1]
	v_mul_f32_e32 v17, 0x37800000, v16
	v_cndmask_b32_e32 v16, v16, v17, vcc
	v_cmp_class_f32_e32 vcc, v7, v1
	s_nop 1
	v_cndmask_b32_e32 v7, v16, v7, vcc
	v_mul_f32_e32 v7, 0x3eb33333, v7
	v_max_f32_e32 v7, 0xda24260, v7
	v_div_scale_f32 v16, s[0:1], v7, v7, 1.0
	v_rcp_f32_e32 v17, v16
	v_div_scale_f32 v28, vcc, 1.0, v7, 1.0
	v_fma_f32 v29, -v16, v17, 1.0
	v_fmac_f32_e32 v17, v29, v17
	v_mul_f32_e32 v29, v28, v17
	v_fma_f32 v30, -v16, v29, v28
	v_fmac_f32_e32 v29, v30, v17
	v_fma_f32 v16, -v16, v29, v28
	v_div_fmas_f32 v16, v16, v17, v29
	v_div_fixup_f32 v16, v16, v7, 1.0
	v_mul_f32_e32 v8, v8, v16
	v_mul_f32_e32 v9, v9, v16
	v_mul_f32_e32 v10, v10, v16
	v_mul_f32_e32 v11, v11, v16
	v_mul_f32_e32 v12, v12, v16
	v_mul_f32_e32 v13, v13, v16
	v_mul_f32_e32 v14, v14, v16
	v_mul_f32_e32 v15, v15, v16
	v_mul_f32_e32 v20, v20, v16
	v_mul_f32_e32 v21, v21, v16
	v_mul_f32_e32 v22, v22, v16
	v_mul_f32_e32 v23, v23, v16
	v_mul_f32_e32 v24, v24, v16
	v_mul_f32_e32 v25, v25, v16
	v_mul_f32_e32 v26, v26, v16
	v_mul_f32_e32 v27, v27, v16
	v_rndne_f32_e32 v8, v8
	v_rndne_f32_e32 v9, v9
	v_rndne_f32_e32 v10, v10
	v_rndne_f32_e32 v11, v11
	v_rndne_f32_e32 v12, v12
	v_rndne_f32_e32 v13, v13
	v_rndne_f32_e32 v14, v14
	v_rndne_f32_e32 v15, v15
	v_rndne_f32_e32 v20, v20
	v_rndne_f32_e32 v21, v21
	v_rndne_f32_e32 v22, v22
	v_rndne_f32_e32 v23, v23
	v_rndne_f32_e32 v24, v24
	v_rndne_f32_e32 v25, v25
	v_rndne_f32_e32 v26, v26
	v_rndne_f32_e32 v27, v27
	v_med3_f32 v8, v8, s13, v6
	v_med3_f32 v9, v9, s13, v6
	v_med3_f32 v10, v10, s13, v6
	v_med3_f32 v11, v11, s13, v6
	v_med3_f32 v12, v12, s13, v6
	v_med3_f32 v13, v13, s13, v6
	v_med3_f32 v14, v14, s13, v6
	v_med3_f32 v15, v15, s13, v6
	v_med3_f32 v20, v20, s13, v6
	v_med3_f32 v21, v21, s13, v6
	v_med3_f32 v22, v22, s13, v6
	v_med3_f32 v23, v23, s13, v6
	v_med3_f32 v24, v24, s13, v6
	v_med3_f32 v25, v25, s13, v6
	v_med3_f32 v26, v26, s13, v6
	v_med3_f32 v27, v27, s13, v6
	v_fmamk_f32 v8, v12, 0x41800000, v8
	v_fmamk_f32 v20, v24, 0x41800000, v20
	v_fmamk_f32 v9, v13, 0x41800000, v9
	v_fmamk_f32 v21, v25, 0x41800000, v21
	v_fmamk_f32 v10, v14, 0x41800000, v10
	v_fmamk_f32 v22, v26, 0x41800000, v22
	v_fmamk_f32 v11, v15, 0x41800000, v11
	v_fmamk_f32 v23, v27, 0x41800000, v23
	v_add_f32_e32 v8, 0x41000000, v8
	v_add_f32_e32 v20, 0x41000000, v20
	v_add_f32_e32 v9, 0x41000000, v9
	v_add_f32_e32 v21, 0x41000000, v21
	v_add_f32_e32 v10, 0x41000000, v10
	v_add_f32_e32 v22, 0x41000000, v22
	v_add_f32_e32 v11, 0x41000000, v11
	v_add_f32_e32 v23, 0x41000000, v23
	v_cvt_i32_f32_e32 v12, v8
	v_cvt_i32_f32_e32 v13, v20
	v_cvt_i32_f32_sdwa v12, v9 dst_sel:BYTE_1 dst_unused:UNUSED_PRESERVE src0_sel:DWORD
	v_cvt_i32_f32_sdwa v13, v21 dst_sel:BYTE_1 dst_unused:UNUSED_PRESERVE src0_sel:DWORD
	v_cvt_i32_f32_sdwa v12, v10 dst_sel:BYTE_2 dst_unused:UNUSED_PRESERVE src0_sel:DWORD
	v_cvt_i32_f32_sdwa v13, v22 dst_sel:BYTE_2 dst_unused:UNUSED_PRESERVE src0_sel:DWORD
	v_cvt_i32_f32_sdwa v12, v11 dst_sel:BYTE_3 dst_unused:UNUSED_PRESERVE src0_sel:DWORD
	v_cvt_i32_f32_sdwa v13, v23 dst_sel:BYTE_3 dst_unused:UNUSED_PRESERVE src0_sel:DWORD
	s_nop 0
	global_store_dwordx2 v[2:3], v[12:13], off
	s_and_saveexec_b64 s[0:1], s[4:5]
	v_mul_f32_e32 v7, 0x3d800000, v7
	global_store_dword v19, v7, s[6:7]
	s_or_b64 exec, exec, s[0:1]
	s_add_u32 s6, s6, s42
	s_addc_u32 s7, s7, s43
	v_lshl_add_u64 v[2:3], v[2:3], 0, s[44:45]
	s_branch .Ltabv_loop

; __device__ __forceinline__ unsigned q4(float x) { return (unsigned)(int)fminf(fmaxf(rintf(x), -7.0f), 7.0f) & 0xfu; }
; __device__ __forceinline__ void cvt_table_i4(const float* src, unsigned char* dst, float* scl, float scl_mul, int gw, int ngw, int lane) {
;     for (int row = gw; row < 16384; row += ngw) {
;         const f32x4* sp = (const f32x4*)(src + (size_t)row * 1024 + 16 * lane);
;         const f32x4 a0 = sp[0], a1 = sp[1], a2 = sp[2], a3 = sp[3];
;         float ss = ((a0.x * a0.x + a0.y * a0.y) + (a0.z * a0.z + a0.w * a0.w)) + ((a1.x * a1.x + a1.y * a1.y) + (a1.z * a1.z + a1.w * a1.w))
;                  + ((a2.x * a2.x + a2.y * a2.y) + (a2.z * a2.z + a2.w * a2.w)) + ((a3.x * a3.x + a3.y * a3.y) + (a3.z * a3.z + a3.w * a3.w));
;         ss = wave_sum(ss);
;         const float step = fmaxf(0.35f * sqrtf(ss * (1.0f / 1024.0f)), 1e-30f), q = 1.0f / step;
;         v2u o;
;         o.x = (q4(a0.x * q) | (q4(a1.x * q) << 4)) | ((q4(a0.y * q) | (q4(a1.y * q) << 4)) << 8) | ((q4(a0.z * q) | (q4(a1.z * q) << 4)) << 16) | ((q4(a0.w * q) | (q4(a1.w * q) << 4)) << 24);
;         o.y = (q4(a2.x * q) | (q4(a3.x * q) << 4)) | ((q4(a2.y * q) | (q4(a3.y * q) << 4)) << 8) | ((q4(a2.z * q) | (q4(a3.z * q) << 4)) << 16) | ((q4(a2.w * q) | (q4(a3.w * q) << 4)) << 24);
;         *(v2u*)(dst + (size_t)row * 512 + 8 * lane) = o;
;         if (lane == 0) scl[row] = step * scl_mul;
;     }
.Ltabv_lastA:
	s_waitcnt vmcnt(2)
	v_mul_f32_e32 v7, v9, v9
	v_mul_f32_e32 v16, v11, v11
	v_mul_f32_e32 v17, v13, v13
	v_mul_f32_e32 v28, v15, v15
	v_mul_f32_e32 v29, v21, v21
	v_mul_f32_e32 v30, v23, v23
	v_fmac_f32_e32 v7, v8, v8
	v_fmac_f32_e32 v16, v10, v10
	v_fmac_f32_e32 v17, v12, v12
	v_fmac_f32_e32 v28, v14, v14
	v_mul_f32_e32 v31, v25, v25
	v_mul_f32_e32 v32, v27, v27
	v_fmac_f32_e32 v29, v20, v20
	v_fmac_f32_e32 v30, v22, v22
	v_add_f32_e32 v7, v7, v16
	v_add_f32_e32 v16, v17, v28
	v_fmac_f32_e32 v31, v24, v24
	v_fmac_f32_e32 v32, v26, v26
	v_add_f32_e32 v17, v29, v30
	v_add_f32_e32 v7, v7, v16
	v_add_f32_e32 v28, v31, v32
	v_add_f32_e32 v7, v7, v17
	v_add_f32_e32 v7, v7, v28
	s_nop 1
	v_add_f32_dpp v7, v7, v7 quad_perm:[1,0,3,2] row_mask:0xf bank_mask:0xf bound_ctrl:1
	s_nop 1
	v_add_f32_dpp v7, v7, v7 quad_perm:[2,3,0,1] row_mask:0xf bank_mask:0xf bound_ctrl:1
	s_nop 1
	v_add_f32_dpp v7, v7, v7 row_half_mirror row_mask:0xf bank_mask:0xf bound_ctrl:1
	s_nop 1
	v_add_f32_dpp v7, v7, v7 row_mirror row_mask:0xf bank_mask:0xf bound_ctrl:1
	v_mov_b32_e32 v16, v7
	s_nop 1
	v_permlane16_swap_b32_e32 v7, v16
	v_add_f32 v7, v7, v16
	s_nop 1
	s_nop 0
	v_mov_b32_e32 v16, v7
	s_nop 1
	v_permlane32_swap_b32_e32 v7, v16
	v_add_f32 v7, v7, v16
	s_nop 0
	v_mul_f32_e32 v7, 0x3a800000, v7
	v_mul_f32_e32 v16, 0x4f800000, v7
	v_cmp_gt_f32_e32 vcc, s3, v7
	s_nop 1
	v_cndmask_b32_e32 v7, v7, v16, vcc
	v_sqrt_f32_e32 v16, v7
	s_nop 0
	v_add_u32_e32 v17, -1, v16
	v_add_u32_e32 v28, 1, v16
	v_fma_f32 v29, -v17, v16, v7
	v_fma_f32 v30, -v28, v16, v7
	v_cmp_ge_f32_e64 s[0:1], 0, v29
	s_nop 1
	v_cndmask_b32_e64 v16, v16, v17, s[0:1]
	v_cmp_lt_f32_e64 s[0:1], 0, v30
	s_nop 1
	v_cndmask_b32_e64 v16, v16, v28, s[0:1]
	v_mul_f32_e32 v17, 0x37800000, v16
	v_cndmask_b32_e32 v16, v16, v17, vcc
	v_cmp_class_f32_e32 vcc, v7, v1
	s_nop 1
	v_cndmask_b32_e32 v7, v16, v7, vcc
	v_mul_f32_e32 v7, 0x3eb33333, v7
	v_max_f32_e32 v7, 0xda24260, v7
	v_div_scale_f32 v16, s[0:1], v7, v7, 1.0
	v_rcp_f32_e32 v17, v16
	v_div_scale_f32 v28, vcc, 1.0, v7, 1.0
	v_fma_f32 v29, -v16, v17, 1.0
	v_fmac_f32_e32 v17, v29, v17
	v_mul_f32_e32 v29, v28, v17
	v_fma_f32 v30, -v16, v29, v28
	v_fmac_f32_e32 v29, v30, v17
	v_fma_f32 v16, -v16, v29, v28
	v_div_fmas_f32 v16, v16, v17, v29
	v_div_fixup_f32 v16, v16, v7, 1.0
	v_mul_f32_e32 v8, v8, v16
	v_mul_f32_e32 v9, v9, v16
	v_mul_f32_e32 v10, v10, v16
	v_mul_f32_e32 v11, v11, v16
	v_mul_f32_e32 v12, v12, v16
	v_mul_f32_e32 v13, v13, v16
	v_mul_f32_e32 v14, v14, v16
	v_mul_f32_e32 v15, v15, v16
	v_mul_f32_e32 v20, v20, v16
	v_mul_f32_e32 v21, v21, v16
	v_mul_f32_e32 v22, v22, v16
	v_mul_f32_e32 v23, v23, v16
	v_mul_f32_e32 v24, v24, v16
	v_mul_f32_e32 v25, v25, v16
	v_mul_f32_e32 v26, v26, v16
	v_mul_f32_e32 v27, v27, v16
	v_rndne_f32_e32 v8, v8
	v_rndne_f32_e32 v9, v9
	v_rndne_f32_e32 v10, v10
	v_rndne_f32_e32 v11, v11
	v_rndne_f32_e32 v12, v12
	v_rndne_f32_e32 v13, v13
	v_rndne_f32_e32 v14, v14
	v_rndne_f32_e32 v15, v15
	v_rndne_f32_e32 v20, v20
	v_rndne_f32_e32 v21, v21
	v_rndne_f32_e32 v22, v22
	v_rndne_f32_e32 v23, v23
	v_rndne_f32_e32 v24, v24
	v_rndne_f32_e32 v25, v25
	v_rndne_f32_e32 v26, v26
	v_rndne_f32_e32 v27, v27
	v_med3_f32 v8, v8, s13, v6
	v_med3_f32 v9, v9, s13, v6
	v_med3_f32 v10, v10, s13, v6
	v_med3_f32 v11, v11, s13, v6
	v_med3_f32 v12, v12, s13, v6
	v_med3_f32 v13, v13, s13, v6
	v_med3_f32 v14, v14, s13, v6
	v_med3_f32 v15, v15, s13, v6
	v_med3_f32 v20, v20, s13, v6
	v_med3_f32 v21, v21, s13, v6
	v_med3_f32 v22, v22, s13, v6
	v_med3_f32 v23, v23, s13, v6
	v_med3_f32 v24, v24, s13, v6
	v_med3_f32 v25, v25, s13, v6
	v_med3_f32 v26, v26, s13, v6
	v_med3_f32 v27, v27, s13, v6
	v_fmamk_f32 v8, v12, 0x41800000, v8
	v_fmamk_f32 v20, v24, 0x41800000, v20
	v_fmamk_f32 v9, v13, 0x41800000, v9
	v_fmamk_f32 v21, v25, 0x41800000, v21
	v_fmamk_f32 v10, v14, 0x41800000, v10
	v_fmamk_f32 v22, v26, 0x41800000, v22
	v_fmamk_f32 v11, v15, 0x41800000, v11
	v_fmamk_f32 v23, v27, 0x41800000, v23
	v_add_f32_e32 v8, 0x41000000, v8
	v_add_f32_e32 v20, 0x41000000, v20
	v_add_f32_e32 v9, 0x41000000, v9
	v_add_f32_e32 v21, 0x41000000, v21
	v_add_f32_e32 v10, 0x41000000, v10
	v_add_f32_e32 v22, 0x41000000, v22
	v_add_f32_e32 v11, 0x41000000, v11
	v_add_f32_e32 v23, 0x41000000, v23
	v_cvt_i32_f32_e32 v12, v8
	v_cvt_i32_f32_e32 v13, v20
	v_cvt_i32_f32_sdwa v12, v9 dst_sel:BYTE_1 dst_unused:UNUSED_PRESERVE src0_sel:DWORD
	v_cvt_i32_f32_sdwa v13, v21 dst_sel:BYTE_1 dst_unused:UNUSED_PRESERVE src0_sel:DWORD
	v_cvt_i32_f32_sdwa v12, v10 dst_sel:BYTE_2 dst_unused:UNUSED_PRESERVE src0_sel:DWORD
	v_cvt_i32_f32_sdwa v13, v22 dst_sel:BYTE_2 dst_unused:UNUSED_PRESERVE src0_sel:DWORD
	v_cvt_i32_f32_sdwa v12, v11 dst_sel:BYTE_3 dst_unused:UNUSED_PRESERVE src0_sel:DWORD
	v_cvt_i32_f32_sdwa v13, v23 dst_sel:BYTE_3 dst_unused:UNUSED_PRESERVE src0_sel:DWORD
	s_nop 0
	global_store_dwordx2 v[2:3], v[12:13], off
	s_and_saveexec_b64 s[0:1], s[4:5]
	v_mul_f32_e32 v7, 0x3d800000, v7
	global_store_dword v19, v7, s[6:7]
	s_or_b64 exec, exec, s[0:1]
	s_branch .LBB0_1975
; __device__ __forceinline__ unsigned q4(float x) { return (unsigned)(int)fminf(fmaxf(rintf(x), -7.0f), 7.0f) & 0xfu; }
; __device__ __forceinline__ void cvt_table_i4(const float* src, unsigned char* dst, float* scl, float scl_mul, int gw, int ngw, int lane) {
;     for (int row = gw; row < 16384; row += ngw) {
;         const f32x4* sp = (const f32x4*)(src + (size_t)row * 1024 + 16 * lane);
;         const f32x4 a0 = sp[0], a1 = sp[1], a2 = sp[2], a3 = sp[3];
;         float ss = ((a0.x * a0.x + a0.y * a0.y) + (a0.z * a0.z + a0.w * a0.w)) + ((a1.x * a1.x + a1.y * a1.y) + (a1.z * a1.z + a1.w * a1.w))
;                  + ((a2.x * a2.x + a2.y * a2.y) + (a2.z * a2.z + a2.w * a2.w)) + ((a3.x * a3.x + a3.y * a3.y) + (a3.z * a3.z + a3.w * a3.w));
;         ss = wave_sum(ss);
;         const float step = fmaxf(0.35f * sqrtf(ss * (1.0f / 1024.0f)), 1e-30f), q = 1.0f / step;
;         v2u o;
;         o.x = (q4(a0.x * q) | (q4(a1.x * q) << 4)) | ((q4(a0.y * q) | (q4(a1.y * q) << 4)) << 8) | ((q4(a0.z * q) | (q4(a1.z * q) << 4)) << 16) | ((q4(a0.w * q) | (q4(a1.w * q) << 4)) << 24);
;         o.y = (q4(a2.x * q) | (q4(a3.x * q) << 4)) | ((q4(a2.y * q) | (q4(a3.y * q) << 4)) << 8) | ((q4(a2.z * q) | (q4(a3.z * q) << 4)) << 16) | ((q4(a2.w * q) | (q4(a3.w * q) << 4)) << 24);
;         *(v2u*)(dst + (size_t)row * 512 + 8 * lane) = o;
;         if (lane == 0) scl[row] = step * scl_mul;
;     }
.Ltabv_lastB:
	s_waitcnt vmcnt(2)
	v_mul_f32_e32 v47, v49, v49
	v_mul_f32_e32 v56, v51, v51
	v_mul_f32_e32 v57, v53, v53
	v_mul_f32_e32 v68, v55, v55
	v_mul_f32_e32 v69, v61, v61
	v_mul_f32_e32 v70, v63, v63
	v_fmac_f32_e32 v47, v48, v48
	v_fmac_f32_e32 v56, v50, v50
	v_fmac_f32_e32 v57, v52, v52
	v_fmac_f32_e32 v68, v54, v54
	v_mul_f32_e32 v71, v65, v65
	v_mul_f32_e32 v72, v67, v67
	v_fmac_f32_e32 v69, v60, v60
	v_fmac_f32_e32 v70, v62, v62
	v_add_f32_e32 v47, v47, v56
	v_add_f32_e32 v56, v57, v68
	v_fmac_f32_e32 v71, v64, v64
	v_fmac_f32_e32 v72, v66, v66
	v_add_f32_e32 v57, v69, v70
	v_add_f32_e32 v47, v47, v56
	v_add_f32_e32 v68, v71, v72
	v_add_f32_e32 v47, v47, v57
	v_add_f32_e32 v47, v47, v68
	s_nop 1
	v_add_f32_dpp v47, v47, v47 quad_perm:[1,0,3,2] row_mask:0xf bank_mask:0xf bound_ctrl:1
	s_nop 1
	v_add_f32_dpp v47, v47, v47 quad_perm:[2,3,0,1] row_mask:0xf bank_mask:0xf bound_ctrl:1
	s_nop 1
	v_add_f32_dpp v47, v47, v47 row_half_mirror row_mask:0xf bank_mask:0xf bound_ctrl:1
	s_nop 1
	v_add_f32_dpp v47, v47, v47 row_mirror row_mask:0xf bank_mask:0xf bound_ctrl:1
	v_mov_b32_e32 v56, v47
	s_nop 1
	v_permlane16_swap_b32_e32 v47, v56
	v_add_f32 v47, v47, v56
	s_nop 1
	s_nop 0
	v_mov_b32_e32 v56, v47
	s_nop 1
	v_permlane32_swap_b32_e32 v47, v56
	v_add_f32 v47, v47, v56
	s_nop 0
	v_mul_f32_e32 v47, 0x3a800000, v47
	v_mul_f32_e32 v56, 0x4f800000, v47
	v_cmp_gt_f32_e32 vcc, s3, v47
	s_nop 1
	v_cndmask_b32_e32 v47, v47, v56, vcc
	v_sqrt_f32_e32 v56, v47
	s_nop 0
	v_add_u32_e32 v57, -1, v56
	v_add_u32_e32 v68, 1, v56
	v_fma_f32 v69, -v57, v56, v47
	v_fma_f32 v70, -v68, v56, v47
	v_cmp_ge_f32_e64 s[0:1], 0, v69
	s_nop 1
	v_cndmask_b32_e64 v56, v56, v57, s[0:1]
	v_cmp_lt_f32_e64 s[0:1], 0, v70
	s_nop 1
	v_cndmask_b32_e64 v56, v56, v68, s[0:1]
	v_mul_f32_e32 v57, 0x37800000, v56
	v_cndmask_b32_e32 v56, v56, v57, vcc
	v_cmp_class_f32_e32 vcc, v47, v1
	s_nop 1
	v_cndmask_b32_e32 v47, v56, v47, vcc
	v_mul_f32_e32 v47, 0x3eb33333, v47
	v_max_f32_e32 v47, 0xda24260, v47
	v_div_scale_f32 v56, s[0:1], v47, v47, 1.0
	v_rcp_f32_e32 v57, v56
	v_div_scale_f32 v68, vcc, 1.0, v47, 1.0
	v_fma_f32 v69, -v56, v57, 1.0
	v_fmac_f32_e32 v57, v69, v57
	v_mul_f32_e32 v69, v68, v57
	v_fma_f32 v70, -v56, v69, v68
	v_fmac_f32_e32 v69, v70, v57
	v_fma_f32 v56, -v56, v69, v68
	v_div_fmas_f32 v56, v56, v57, v69
	v_div_fixup_f32 v56, v56, v47, 1.0
	v_mul_f32_e32 v48, v48, v56
	v_mul_f32_e32 v49, v49, v56
	v_mul_f32_e32 v50, v50, v56
	v_mul_f32_e32 v51, v51, v56
	v_mul_f32_e32 v52, v52, v56
	v_mul_f32_e32 v53, v53, v56
	v_mul_f32_e32 v54, v54, v56
	v_mul_f32_e32 v55, v55, v56
	v_mul_f32_e32 v60, v60, v56
	v_mul_f32_e32 v61, v61, v56
	v_mul_f32_e32 v62, v62, v56
	v_mul_f32_e32 v63, v63, v56
	v_mul_f32_e32 v64, v64, v56
	v_mul_f32_e32 v65, v65, v56
	v_mul_f32_e32 v66, v66, v56
	v_mul_f32_e32 v67, v67, v56
	v_rndne_f32_e32 v48, v48
	v_rndne_f32_e32 v49, v49
	v_rndne_f32_e32 v50, v50
	v_rndne_f32_e32 v51, v51
	v_rndne_f32_e32 v52, v52
	v_rndne_f32_e32 v53, v53
	v_rndne_f32_e32 v54, v54
	v_rndne_f32_e32 v55, v55
	v_rndne_f32_e32 v60, v60
	v_rndne_f32_e32 v61, v61
	v_rndne_f32_e32 v62, v62
	v_rndne_f32_e32 v63, v63
	v_rndne_f32_e32 v64, v64
	v_rndne_f32_e32 v65, v65
	v_rndne_f32_e32 v66, v66
	v_rndne_f32_e32 v67, v67
	v_med3_f32 v48, v48, s13, v6
	v_med3_f32 v49, v49, s13, v6
	v_med3_f32 v50, v50, s13, v6
	v_med3_f32 v51, v51, s13, v6
	v_med3_f32 v52, v52, s13, v6
	v_med3_f32 v53, v53, s13, v6
	v_med3_f32 v54, v54, s13, v6
	v_med3_f32 v55, v55, s13, v6
	v_med3_f32 v60, v60, s13, v6
	v_med3_f32 v61, v61, s13, v6
	v_med3_f32 v62, v62, s13, v6
	v_med3_f32 v63, v63, s13, v6
	v_med3_f32 v64, v64, s13, v6
	v_med3_f32 v65, v65, s13, v6
	v_med3_f32 v66, v66, s13, v6
	v_med3_f32 v67, v67, s13, v6
	v_fmamk_f32 v48, v52, 0x41800000, v48
	v_fmamk_f32 v60, v64, 0x41800000, v60
	v_fmamk_f32 v49, v53, 0x41800000, v49
	v_fmamk_f32 v61, v65, 0x41800000, v61
	v_fmamk_f32 v50, v54, 0x41800000, v50
	v_fmamk_f32 v62, v66, 0x41800000, v62
	v_fmamk_f32 v51, v55, 0x41800000, v51
	v_fmamk_f32 v63, v67, 0x41800000, v63
	v_add_f32_e32 v48, 0x41000000, v48
	v_add_f32_e32 v60, 0x41000000, v60
	v_add_f32_e32 v49, 0x41000000, v49
	v_add_f32_e32 v61, 0x41000000, v61
	v_add_f32_e32 v50, 0x41000000, v50
	v_add_f32_e32 v62, 0x41000000, v62
	v_add_f32_e32 v51, 0x41000000, v51
	v_add_f32_e32 v63, 0x41000000, v63
	v_cvt_i32_f32_e32 v52, v48
	v_cvt_i32_f32_e32 v53, v60
	v_cvt_i32_f32_sdwa v52, v49 dst_sel:BYTE_1 dst_unused:UNUSED_PRESERVE src0_sel:DWORD
	v_cvt_i32_f32_sdwa v53, v61 dst_sel:BYTE_1 dst_unused:UNUSED_PRESERVE src0_sel:DWORD
	v_cvt_i32_f32_sdwa v52, v50 dst_sel:BYTE_2 dst_unused:UNUSED_PRESERVE src0_sel:DWORD
	v_cvt_i32_f32_sdwa v53, v62 dst_sel:BYTE_2 dst_unused:UNUSED_PRESERVE src0_sel:DWORD
	v_cvt_i32_f32_sdwa v52, v51 dst_sel:BYTE_3 dst_unused:UNUSED_PRESERVE src0_sel:DWORD
	v_cvt_i32_f32_sdwa v53, v63 dst_sel:BYTE_3 dst_unused:UNUSED_PRESERVE src0_sel:DWORD
	s_nop 0
	global_store_dwordx2 v[2:3], v[52:53], off
	s_and_saveexec_b64 s[0:1], s[4:5]
	v_mul_f32_e32 v47, 0x3d800000, v47
	global_store_dword v19, v47, s[6:7]
	s_or_b64 exec, exec, s[0:1]

; __device__ __forceinline__ unsigned q4(float x) { return (unsigned)(int)fminf(fmaxf(rintf(x), -7.0f), 7.0f) & 0xfu; }
; __device__ __forceinline__ void cvt_table_i4(const float* src, unsigned char* dst, float* scl, float scl_mul, int gw, int ngw, int lane) {
;     for (int row = gw; row < 16384; row += ngw) {
;         const f32x4* sp = (const f32x4*)(src + (size_t)row * 1024 + 16 * lane);
;         const f32x4 a0 = sp[0], a1 = sp[1], a2 = sp[2], a3 = sp[3];
;         float ss = ((a0.x * a0.x + a0.y * a0.y) + (a0.z * a0.z + a0.w * a0.w)) + ((a1.x * a1.x + a1.y * a1.y) + (a1.z * a1.z + a1.w * a1.w))
;                  + ((a2.x * a2.x + a2.y * a2.y) + (a2.z * a2.z + a2.w * a2.w)) + ((a3.x * a3.x + a3.y * a3.y) + (a3.z * a3.z + a3.w * a3.w));
;         ss = wave_sum(ss);
;         const float step = fmaxf(0.35f * sqrtf(ss * (1.0f / 1024.0f)), 1e-30f), q = 1.0f / step;
;         v2u o;
;         o.x = (q4(a0.x * q) | (q4(a1.x * q) << 4)) | ((q4(a0.y * q) | (q4(a1.y * q) << 4)) << 8) | ((q4(a0.z * q) | (q4(a1.z * q) << 4)) << 16) | ((q4(a0.w * q) | (q4(a1.w * q) << 4)) << 24);
;         o.y = (q4(a2.x * q) | (q4(a3.x * q) << 4)) | ((q4(a2.y * q) | (q4(a3.y * q) << 4)) << 8) | ((q4(a2.z * q) | (q4(a3.z * q) << 4)) << 16) | ((q4(a2.w * q) | (q4(a3.w * q) << 4)) << 24);
;         *(v2u*)(dst + (size_t)row * 512 + 8 * lane) = o;
;         if (lane == 0) scl[row] = step * scl_mul;
;     }
.LBB0_2025:
	global_load_dwordx4 v[10:13], v[6:7], off offset:-32
	global_load_dwordx4 v[14:17], v[6:7], off offset:-16
	global_load_dwordx4 v[18:21], v[6:7], off
	global_load_dwordx4 v[22:25], v[6:7], off offset:16
	s_add_i32 s16, s16, s18
	v_lshl_add_u64 v[6:7], v[6:7], 0, s[44:45]
	s_cmpk_lt_i32 s16, 0x4000
	s_cbranch_scc0 .Ltabu_lastA0
	global_load_dwordx4 v[50:53], v[6:7], off offset:-32
	global_load_dwordx4 v[54:57], v[6:7], off offset:-16
	global_load_dwordx4 v[58:61], v[6:7], off
	global_load_dwordx4 v[62:65], v[6:7], off offset:16
	s_waitcnt vmcnt(4)
	v_mul_f32_e32 v8, v11, v11
	v_mul_f32_e32 v9, v13, v13
	v_mul_f32_e32 v26, v15, v15
	v_mul_f32_e32 v27, v17, v17
	v_mul_f32_e32 v28, v19, v19
	v_mul_f32_e32 v29, v21, v21
	v_fmac_f32_e32 v8, v10, v10
	v_fmac_f32_e32 v9, v12, v12
	v_fmac_f32_e32 v26, v14, v14
	v_fmac_f32_e32 v27, v16, v16
	v_mul_f32_e32 v30, v23, v23
	v_mul_f32_e32 v31, v25, v25
	v_fmac_f32_e32 v28, v18, v18
	v_fmac_f32_e32 v29, v20, v20
	v_add_f32_e32 v8, v8, v9
	v_add_f32_e32 v9, v26, v27
	v_fmac_f32_e32 v30, v22, v22
	v_fmac_f32_e32 v31, v24, v24
	v_add_f32_e32 v26, v28, v29
	v_add_f32_e32 v8, v8, v9
	v_add_f32_e32 v27, v30, v31
	v_add_f32_e32 v8, v8, v26
	v_add_f32_e32 v8, v8, v27
	s_nop 1
	v_add_f32_dpp v8, v8, v8 quad_perm:[1,0,3,2] row_mask:0xf bank_mask:0xf bound_ctrl:1
	s_nop 1
	v_add_f32_dpp v8, v8, v8 quad_perm:[2,3,0,1] row_mask:0xf bank_mask:0xf bound_ctrl:1
	s_nop 1
	v_add_f32_dpp v8, v8, v8 row_half_mirror row_mask:0xf bank_mask:0xf bound_ctrl:1
	s_nop 1
	v_add_f32_dpp v8, v8, v8 row_mirror row_mask:0xf bank_mask:0xf bound_ctrl:1
	v_mov_b32_e32 v9, v8
	s_nop 1
	v_permlane16_swap_b32_e32 v8, v9
	v_add_f32 v8, v8, v9
	s_nop 1
	s_nop 0
	v_mov_b32_e32 v9, v8
	s_nop 1
	v_permlane32_swap_b32_e32 v8, v9
	v_add_f32 v8, v8, v9
	s_nop 0
	v_mul_f32_e32 v8, 0x3a800000, v8
	v_mul_f32_e32 v9, 0x4f800000, v8
	v_cmp_gt_f32_e32 vcc, s3, v8
	s_nop 1
	v_cndmask_b32_e32 v8, v8, v9, vcc
	v_sqrt_f32_e32 v9, v8
	s_nop 0
	v_add_u32_e32 v26, -1, v9
	v_add_u32_e32 v27, 1, v9
	v_fma_f32 v28, -v26, v9, v8
	v_fma_f32 v29, -v27, v9, v8
	v_cmp_ge_f32_e64 s[0:1], 0, v28
	s_nop 1
	v_cndmask_b32_e64 v9, v9, v26, s[0:1]
	v_cmp_lt_f32_e64 s[0:1], 0, v29
	s_nop 1
	v_cndmask_b32_e64 v9, v9, v27, s[0:1]
	v_mul_f32_e32 v26, 0x37800000, v9
	v_cndmask_b32_e32 v9, v9, v26, vcc
	v_cmp_class_f32_e32 vcc, v8, v1
	s_nop 1
	v_cndmask_b32_e32 v8, v9, v8, vcc
	v_mul_f32_e32 v8, 0x3eb33333, v8
	v_max_f32_e32 v8, 0xda24260, v8
	v_div_scale_f32 v9, s[0:1], v8, v8, 1.0
	v_rcp_f32_e32 v26, v9
	v_div_scale_f32 v27, vcc, 1.0, v8, 1.0
	v_fma_f32 v28, -v9, v26, 1.0
	v_fmac_f32_e32 v26, v28, v26
	v_mul_f32_e32 v28, v27, v26
	v_fma_f32 v29, -v9, v28, v27
	v_fmac_f32_e32 v28, v29, v26
	v_fma_f32 v9, -v9, v28, v27
	v_div_fmas_f32 v9, v9, v26, v28
	v_div_fixup_f32 v9, v9, v8, 1.0
	v_mul_f32_e32 v10, v10, v9
	v_mul_f32_e32 v12, v12, v9
	v_mul_f32_e32 v16, v16, v9
	v_mul_f32_e32 v17, v17, v9
	v_mul_f32_e32 v11, v11, v9
	v_mul_f32_e32 v15, v15, v9
	v_mul_f32_e32 v13, v13, v9
	v_rndne_f32_e32 v10, v10
	v_rndne_f32_e32 v12, v12
	v_rndne_f32_e32 v16, v16
	v_rndne_f32_e32 v17, v17
	v_mul_f32_e32 v14, v14, v9
	v_rndne_f32_e32 v11, v11
	v_rndne_f32_e32 v15, v15
	v_rndne_f32_e32 v13, v13
	v_med3_f32 v10, v10, s13, v4
	v_med3_f32 v12, v12, s13, v4
	v_med3_f32 v16, v16, s13, v4
	v_med3_f32 v17, v17, s13, v4
	v_rndne_f32_e32 v14, v14
	v_med3_f32 v11, v11, s13, v4
	v_med3_f32 v15, v15, s13, v4
	v_med3_f32 v13, v13, s13, v4
	v_cvt_i32_f32_e32 v10, v10
	v_cvt_i32_f32_sdwa v12, v12 dst_sel:WORD_1 dst_unused:UNUSED_PAD src0_sel:DWORD
	v_cvt_i32_f32_e32 v16, v16
	v_cvt_i32_f32_e32 v17, v17
	v_med3_f32 v14, v14, s13, v4
	v_cvt_i32_f32_e32 v11, v11
	v_cvt_i32_f32_e32 v15, v15
	v_cvt_i32_f32_sdwa v13, v13 dst_sel:BYTE_3 dst_unused:UNUSED_PAD src0_sel:DWORD
	v_cvt_i32_f32_e32 v14, v14
	v_and_b32_e32 v10, 15, v10
	v_lshlrev_b32_e32 v16, 20, v16
	v_and_b32_e32 v12, 0xf0000, v12
	v_lshlrev_b32_e32 v17, 28, v17
	v_lshlrev_b32_e32 v15, 12, v15
	v_lshlrev_b32_e32 v11, 8, v11
	v_and_b32_e32 v13, 0xf000000, v13
	v_and_b32_e32 v16, 0xf00000, v16
	v_or3_b32 v10, v10, v17, v12
	v_lshlrev_b32_e32 v14, 4, v14
	v_and_b32_e32 v15, 0xf000, v15
	v_and_b32_e32 v11, 0xf00, v11
	v_or3_b32 v10, v10, v16, v13
	v_and_b32_e32 v14, 0xf0, v14
	v_or3_b32 v10, v10, v11, v15
	v_mul_f32_e32 v18, v18, v9
	v_mul_f32_e32 v22, v22, v9
	v_mul_f32_e32 v19, v19, v9
	v_mul_f32_e32 v23, v23, v9
	v_add_u32_e32 v10, v10, v14
	v_mul_f32_e32 v14, v20, v9
	v_mul_f32_e32 v15, v24, v9
	v_mul_f32_e32 v16, v21, v9
	v_mul_f32_e32 v9, v25, v9
	v_rndne_f32_e32 v18, v18
	v_rndne_f32_e32 v15, v15
	v_rndne_f32_e32 v14, v14
	v_rndne_f32_e32 v9, v9
	v_rndne_f32_e32 v19, v19
	v_rndne_f32_e32 v23, v23
	v_med3_f32 v18, v18, s13, v4
	v_med3_f32 v15, v15, s13, v4
	v_med3_f32 v14, v14, s13, v4
	v_rndne_f32_e32 v16, v16
	v_med3_f32 v9, v9, s13, v4
	v_rndne_f32_e32 v22, v22
	v_med3_f32 v19, v19, s13, v4
	v_med3_f32 v23, v23, s13, v4
	v_cvt_i32_f32_e32 v18, v18
	v_cvt_i32_f32_e32 v15, v15
	v_cvt_i32_f32_sdwa v14, v14 dst_sel:WORD_1 dst_unused:UNUSED_PAD src0_sel:DWORD
	v_med3_f32 v16, v16, s13, v4
	v_cvt_i32_f32_e32 v9, v9
	v_med3_f32 v22, v22, s13, v4
	v_cvt_i32_f32_e32 v23, v23
	v_cvt_i32_f32_e32 v11, v19
	v_cvt_i32_f32_sdwa v16, v16 dst_sel:BYTE_3 dst_unused:UNUSED_PAD src0_sel:DWORD
	v_cvt_i32_f32_e32 v22, v22
	v_and_b32_e32 v18, 15, v18
	v_lshlrev_b32_e32 v15, 20, v15
	v_and_b32_e32 v14, 0xf0000, v14
	v_lshlrev_b32_e32 v9, 28, v9
	v_lshlrev_b32_e32 v13, 12, v23
	v_lshlrev_b32_e32 v11, 8, v11
	v_and_b32_e32 v15, 0xf00000, v15
	v_and_b32_e32 v16, 0xf000000, v16
	v_or3_b32 v9, v18, v9, v14
	v_lshlrev_b32_e32 v22, 4, v22
	v_and_b32_e32 v13, 0xf000, v13
	v_and_b32_e32 v11, 0xf00, v11
	v_or3_b32 v9, v9, v15, v16
	v_and_b32_e32 v12, 0xf0, v22
	v_or3_b32 v9, v9, v11, v13
	v_add_u32_e32 v11, v9, v12
	global_store_dwordx2 v[2:3], v[10:11], off
	s_and_saveexec_b64 s[0:1], s[4:5]
	global_store_dword v5, v8, s[6:7]
	s_or_b64 exec, exec, s[0:1]
	s_add_u32 s6, s6, s20
	s_addc_u32 s7, s7, s21
	v_lshl_add_u64 v[2:3], v[2:3], 0, s[42:43]
; __device__ __forceinline__ unsigned q4(float x) { return (unsigned)(int)fminf(fmaxf(rintf(x), -7.0f), 7.0f) & 0xfu; }
; __device__ __forceinline__ void cvt_table_i4(const float* src, unsigned char* dst, float* scl, float scl_mul, int gw, int ngw, int lane) {
;     for (int row = gw; row < 16384; row += ngw) {
;         const f32x4* sp = (const f32x4*)(src + (size_t)row * 1024 + 16 * lane);
;         const f32x4 a0 = sp[0], a1 = sp[1], a2 = sp[2], a3 = sp[3];
;         float ss = ((a0.x * a0.x + a0.y * a0.y) + (a0.z * a0.z + a0.w * a0.w)) + ((a1.x * a1.x + a1.y * a1.y) + (a1.z * a1.z + a1.w * a1.w))
;                  + ((a2.x * a2.x + a2.y * a2.y) + (a2.z * a2.z + a2.w * a2.w)) + ((a3.x * a3.x + a3.y * a3.y) + (a3.z * a3.z + a3.w * a3.w));
;         ss = wave_sum(ss);
;         const float step = fmaxf(0.35f * sqrtf(ss * (1.0f / 1024.0f)), 1e-30f), q = 1.0f / step;
;         v2u o;
;         o.x = (q4(a0.x * q) | (q4(a1.x * q) << 4)) | ((q4(a0.y * q) | (q4(a1.y * q) << 4)) << 8) | ((q4(a0.z * q) | (q4(a1.z * q) << 4)) << 16) | ((q4(a0.w * q) | (q4(a1.w * q) << 4)) << 24);
;         o.y = (q4(a2.x * q) | (q4(a3.x * q) << 4)) | ((q4(a2.y * q) | (q4(a3.y * q) << 4)) << 8) | ((q4(a2.z * q) | (q4(a3.z * q) << 4)) << 16) | ((q4(a2.w * q) | (q4(a3.w * q) << 4)) << 24);
;         *(v2u*)(dst + (size_t)row * 512 + 8 * lane) = o;
;         if (lane == 0) scl[row] = step * scl_mul;
;     }
.Ltabu_loop:
	s_add_i32 s16, s16, s18
	v_lshl_add_u64 v[6:7], v[6:7], 0, s[44:45]
	s_cmpk_lt_i32 s16, 0x4000
	s_cbranch_scc0 .Ltabu_lastB
	global_load_dwordx4 v[10:13], v[6:7], off offset:-32
	global_load_dwordx4 v[14:17], v[6:7], off offset:-16
	global_load_dwordx4 v[18:21], v[6:7], off
	global_load_dwordx4 v[22:25], v[6:7], off offset:16
	s_waitcnt vmcnt(6)
	v_mul_f32_e32 v48, v51, v51
	v_mul_f32_e32 v49, v53, v53
	v_mul_f32_e32 v66, v55, v55
	v_mul_f32_e32 v67, v57, v57
	v_mul_f32_e32 v68, v59, v59
	v_mul_f32_e32 v69, v61, v61
	v_fmac_f32_e32 v48, v50, v50
	v_fmac_f32_e32 v49, v52, v52
	v_fmac_f32_e32 v66, v54, v54
	v_fmac_f32_e32 v67, v56, v56
	v_mul_f32_e32 v70, v63, v63
	v_mul_f32_e32 v71, v65, v65
	v_fmac_f32_e32 v68, v58, v58
	v_fmac_f32_e32 v69, v60, v60
	v_add_f32_e32 v48, v48, v49
	v_add_f32_e32 v49, v66, v67
	v_fmac_f32_e32 v70, v62, v62
	v_fmac_f32_e32 v71, v64, v64
	v_add_f32_e32 v66, v68, v69
	v_add_f32_e32 v48, v48, v49
	v_add_f32_e32 v67, v70, v71
	v_add_f32_e32 v48, v48, v66
	v_add_f32_e32 v48, v48, v67
	s_nop 1
	v_add_f32_dpp v48, v48, v48 quad_perm:[1,0,3,2] row_mask:0xf bank_mask:0xf bound_ctrl:1
	s_nop 1
	v_add_f32_dpp v48, v48, v48 quad_perm:[2,3,0,1] row_mask:0xf bank_mask:0xf bound_ctrl:1
	s_nop 1
	v_add_f32_dpp v48, v48, v48 row_half_mirror row_mask:0xf bank_mask:0xf bound_ctrl:1
	s_nop 1
	v_add_f32_dpp v48, v48, v48 row_mirror row_mask:0xf bank_mask:0xf bound_ctrl:1
	v_mov_b32_e32 v49, v48
	s_nop 1
	v_permlane16_swap_b32_e32 v48, v49
	v_add_f32 v48, v48, v49
	s_nop 1
	s_nop 0
	v_mov_b32_e32 v49, v48
	s_nop 1
	v_permlane32_swap_b32_e32 v48, v49
	v_add_f32 v48, v48, v49
	s_nop 0
	v_mul_f32_e32 v48, 0x3a800000, v48
	v_mul_f32_e32 v49, 0x4f800000, v48
	v_cmp_gt_f32_e32 vcc, s3, v48
	s_nop 1
	v_cndmask_b32_e32 v48, v48, v49, vcc
	v_sqrt_f32_e32 v49, v48
	s_nop 0
	v_add_u32_e32 v66, -1, v49
	v_add_u32_e32 v67, 1, v49
	v_fma_f32 v68, -v66, v49, v48
	v_fma_f32 v69, -v67, v49, v48
	v_cmp_ge_f32_e64 s[0:1], 0, v68
	s_nop 1
	v_cndmask_b32_e64 v49, v49, v66, s[0:1]
	v_cmp_lt_f32_e64 s[0:1], 0, v69
	s_nop 1
	v_cndmask_b32_e64 v49, v49, v67, s[0:1]
	v_mul_f32_e32 v66, 0x37800000, v49
	v_cndmask_b32_e32 v49, v49, v66, vcc
	v_cmp_class_f32_e32 vcc, v48, v1
	s_nop 1
	v_cndmask_b32_e32 v48, v49, v48, vcc
	v_mul_f32_e32 v48, 0x3eb33333, v48
	v_max_f32_e32 v48, 0xda24260, v48
	v_div_scale_f32 v49, s[0:1], v48, v48, 1.0
	v_rcp_f32_e32 v66, v49
	v_div_scale_f32 v67, vcc, 1.0, v48, 1.0
	v_fma_f32 v68, -v49, v66, 1.0
	v_fmac_f32_e32 v66, v68, v66
	v_mul_f32_e32 v68, v67, v66
	v_fma_f32 v69, -v49, v68, v67
	v_fmac_f32_e32 v68, v69, v66
	v_fma_f32 v49, -v49, v68, v67
	v_div_fmas_f32 v49, v49, v66, v68
	v_div_fixup_f32 v49, v49, v48, 1.0
	v_mul_f32_e32 v50, v50, v49
	v_mul_f32_e32 v52, v52, v49
	v_mul_f32_e32 v56, v56, v49
	v_mul_f32_e32 v57, v57, v49
	v_mul_f32_e32 v51, v51, v49
	v_mul_f32_e32 v55, v55, v49
	v_mul_f32_e32 v53, v53, v49
	v_rndne_f32_e32 v50, v50
	v_rndne_f32_e32 v52, v52
	v_rndne_f32_e32 v56, v56
	v_rndne_f32_e32 v57, v57
	v_mul_f32_e32 v54, v54, v49
	v_rndne_f32_e32 v51, v51
	v_rndne_f32_e32 v55, v55
	v_rndne_f32_e32 v53, v53
	v_med3_f32 v50, v50, s13, v4
	v_med3_f32 v52, v52, s13, v4
	v_med3_f32 v56, v56, s13, v4
	v_med3_f32 v57, v57, s13, v4
	v_rndne_f32_e32 v54, v54
	v_med3_f32 v51, v51, s13, v4
	v_med3_f32 v55, v55, s13, v4
	v_med3_f32 v53, v53, s13, v4
	v_cvt_i32_f32_e32 v50, v50
	v_cvt_i32_f32_sdwa v52, v52 dst_sel:WORD_1 dst_unused:UNUSED_PAD src0_sel:DWORD
	v_cvt_i32_f32_e32 v56, v56
	v_cvt_i32_f32_e32 v57, v57
	v_med3_f32 v54, v54, s13, v4
	v_cvt_i32_f32_e32 v51, v51
	v_cvt_i32_f32_e32 v55, v55
	v_cvt_i32_f32_sdwa v53, v53 dst_sel:BYTE_3 dst_unused:UNUSED_PAD src0_sel:DWORD
	v_cvt_i32_f32_e32 v54, v54
	v_and_b32_e32 v50, 15, v50
	v_lshlrev_b32_e32 v56, 20, v56
	v_and_b32_e32 v52, 0xf0000, v52
	v_lshlrev_b32_e32 v57, 28, v57
	v_lshlrev_b32_e32 v55, 12, v55
	v_lshlrev_b32_e32 v51, 8, v51
	v_and_b32_e32 v53, 0xf000000, v53
	v_and_b32_e32 v56, 0xf00000, v56
	v_or3_b32 v50, v50, v57, v52
	v_lshlrev_b32_e32 v54, 4, v54
	v_and_b32_e32 v55, 0xf000, v55
	v_and_b32_e32 v51, 0xf00, v51
	v_or3_b32 v50, v50, v56, v53
	v_and_b32_e32 v54, 0xf0, v54
	v_or3_b32 v50, v50, v51, v55
	v_mul_f32_e32 v58, v58, v49
	v_mul_f32_e32 v62, v62, v49
	v_mul_f32_e32 v59, v59, v49
	v_mul_f32_e32 v63, v63, v49
	v_add_u32_e32 v50, v50, v54
	v_mul_f32_e32 v54, v60, v49
	v_mul_f32_e32 v55, v64, v49
	v_mul_f32_e32 v56, v61, v49
	v_mul_f32_e32 v49, v65, v49
	v_rndne_f32_e32 v58, v58
	v_rndne_f32_e32 v55, v55
	v_rndne_f32_e32 v54, v54
	v_rndne_f32_e32 v49, v49
	v_rndne_f32_e32 v59, v59
	v_rndne_f32_e32 v63, v63
	v_med3_f32 v58, v58, s13, v4
	v_med3_f32 v55, v55, s13, v4
	v_med3_f32 v54, v54, s13, v4
	v_rndne_f32_e32 v56, v56
	v_med3_f32 v49, v49, s13, v4
	v_rndne_f32_e32 v62, v62
	v_med3_f32 v59, v59, s13, v4
	v_med3_f32 v63, v63, s13, v4
	v_cvt_i32_f32_e32 v58, v58
	v_cvt_i32_f32_e32 v55, v55
	v_cvt_i32_f32_sdwa v54, v54 dst_sel:WORD_1 dst_unused:UNUSED_PAD src0_sel:DWORD
	v_med3_f32 v56, v56, s13, v4
	v_cvt_i32_f32_e32 v49, v49
	v_med3_f32 v62, v62, s13, v4
	v_cvt_i32_f32_e32 v63, v63
	v_cvt_i32_f32_e32 v51, v59
	v_cvt_i32_f32_sdwa v56, v56 dst_sel:BYTE_3 dst_unused:UNUSED_PAD src0_sel:DWORD
	v_cvt_i32_f32_e32 v62, v62
	v_and_b32_e32 v58, 15, v58
	v_lshlrev_b32_e32 v55, 20, v55
	v_and_b32_e32 v54, 0xf0000, v54
	v_lshlrev_b32_e32 v49, 28, v49
	v_lshlrev_b32_e32 v53, 12, v63
	v_lshlrev_b32_e32 v51, 8, v51
	v_and_b32_e32 v55, 0xf00000, v55
	v_and_b32_e32 v56, 0xf000000, v56
	v_or3_b32 v49, v58, v49, v54
	v_lshlrev_b32_e32 v62, 4, v62
	v_and_b32_e32 v53, 0xf000, v53
	v_and_b32_e32 v51, 0xf00, v51
	v_or3_b32 v49, v49, v55, v56
	v_and_b32_e32 v52, 0xf0, v62
	v_or3_b32 v49, v49, v51, v53
	v_add_u32_e32 v51, v49, v52
	global_store_dwordx2 v[2:3], v[50:51], off
	s_and_saveexec_b64 s[0:1], s[4:5]
	global_store_dword v5, v48, s[6:7]
	s_or_b64 exec, exec, s[0:1]
	s_add_u32 s6, s6, s20
	s_addc_u32 s7, s7, s21
	v_lshl_add_u64 v[2:3], v[2:3], 0, s[42:43]
	s_add_i32 s16, s16, s18
	v_lshl_add_u64 v[6:7], v[6:7], 0, s[44:45]
	s_cmpk_lt_i32 s16, 0x4000
	s_cbranch_scc0 .Ltabu_lastA
; __device__ __forceinline__ unsigned q4(float x) { return (unsigned)(int)fminf(fmaxf(rintf(x), -7.0f), 7.0f) & 0xfu; }
; __device__ __forceinline__ void cvt_table_i4(const float* src, unsigned char* dst, float* scl, float scl_mul, int gw, int ngw, int lane) {
;     for (int row = gw; row < 16384; row += ngw) {
;         const f32x4* sp = (const f32x4*)(src + (size_t)row * 1024 + 16 * lane);
;         const f32x4 a0 = sp[0], a1 = sp[1], a2 = sp[2], a3 = sp[3];
;         float ss = ((a0.x * a0.x + a0.y * a0.y) + (a0.z * a0.z + a0.w * a0.w)) + ((a1.x * a1.x + a1.y * a1.y) + (a1.z * a1.z + a1.w * a1.w))
;                  + ((a2.x * a2.x + a2.y * a2.y) + (a2.z * a2.z + a2.w * a2.w)) + ((a3.x * a3.x + a3.y * a3.y) + (a3.z * a3.z + a3.w * a3.w));
;         ss = wave_sum(ss);
;         const float step = fmaxf(0.35f * sqrtf(ss * (1.0f / 1024.0f)), 1e-30f), q = 1.0f / step;
;         v2u o;
;         o.x = (q4(a0.x * q) | (q4(a1.x * q) << 4)) | ((q4(a0.y * q) | (q4(a1.y * q) << 4)) << 8) | ((q4(a0.z * q) | (q4(a1.z * q) << 4)) << 16) | ((q4(a0.w * q) | (q4(a1.w * q) << 4)) << 24);
;         o.y = (q4(a2.x * q) | (q4(a3.x * q) << 4)) | ((q4(a2.y * q) | (q4(a3.y * q) << 4)) << 8) | ((q4(a2.z * q) | (q4(a3.z * q) << 4)) << 16) | ((q4(a2.w * q) | (q4(a3.w * q) << 4)) << 24);
;         *(v2u*)(dst + (size_t)row * 512 + 8 * lane) = o;
;         if (lane == 0) scl[row] = step * scl_mul;
;     }
	global_load_dwordx4 v[50:53], v[6:7], off offset:-32
	global_load_dwordx4 v[54:57], v[6:7], off offset:-16
	global_load_dwordx4 v[58:61], v[6:7], off
	global_load_dwordx4 v[62:65], v[6:7], off offset:16
	s_waitcnt vmcnt(6)
	v_mul_f32_e32 v8, v11, v11
	v_mul_f32_e32 v9, v13, v13
	v_mul_f32_e32 v26, v15, v15
	v_mul_f32_e32 v27, v17, v17
	v_mul_f32_e32 v28, v19, v19
	v_mul_f32_e32 v29, v21, v21
	v_fmac_f32_e32 v8, v10, v10
	v_fmac_f32_e32 v9, v12, v12
	v_fmac_f32_e32 v26, v14, v14
	v_fmac_f32_e32 v27, v16, v16
	v_mul_f32_e32 v30, v23, v23
	v_mul_f32_e32 v31, v25, v25
	v_fmac_f32_e32 v28, v18, v18
	v_fmac_f32_e32 v29, v20, v20
	v_add_f32_e32 v8, v8, v9
	v_add_f32_e32 v9, v26, v27
	v_fmac_f32_e32 v30, v22, v22
	v_fmac_f32_e32 v31, v24, v24
	v_add_f32_e32 v26, v28, v29
	v_add_f32_e32 v8, v8, v9
	v_add_f32_e32 v27, v30, v31
	v_add_f32_e32 v8, v8, v26
	v_add_f32_e32 v8, v8, v27
	s_nop 1
	v_add_f32_dpp v8, v8, v8 quad_perm:[1,0,3,2] row_mask:0xf bank_mask:0xf bound_ctrl:1
	s_nop 1
	v_add_f32_dpp v8, v8, v8 quad_perm:[2,3,0,1] row_mask:0xf bank_mask:0xf bound_ctrl:1
	s_nop 1
	v_add_f32_dpp v8, v8, v8 row_half_mirror row_mask:0xf bank_mask:0xf bound_ctrl:1
	s_nop 1
	v_add_f32_dpp v8, v8, v8 row_mirror row_mask:0xf bank_mask:0xf bound_ctrl:1
	v_mov_b32_e32 v9, v8
	s_nop 1
	v_permlane16_swap_b32_e32 v8, v9
	v_add_f32 v8, v8, v9
	s_nop 1
	s_nop 0
	v_mov_b32_e32 v9, v8
	s_nop 1
	v_permlane32_swap_b32_e32 v8, v9
	v_add_f32 v8, v8, v9
	s_nop 0
	v_mul_f32_e32 v8, 0x3a800000, v8
	v_mul_f32_e32 v9, 0x4f800000, v8
	v_cmp_gt_f32_e32 vcc, s3, v8
	s_nop 1
	v_cndmask_b32_e32 v8, v8, v9, vcc
	v_sqrt_f32_e32 v9, v8
	s_nop 0
	v_add_u32_e32 v26, -1, v9
	v_add_u32_e32 v27, 1, v9
	v_fma_f32 v28, -v26, v9, v8
	v_fma_f32 v29, -v27, v9, v8
	v_cmp_ge_f32_e64 s[0:1], 0, v28
	s_nop 1
	v_cndmask_b32_e64 v9, v9, v26, s[0:1]
	v_cmp_lt_f32_e64 s[0:1], 0, v29
	s_nop 1
	v_cndmask_b32_e64 v9, v9, v27, s[0:1]
	v_mul_f32_e32 v26, 0x37800000, v9
	v_cndmask_b32_e32 v9, v9, v26, vcc
	v_cmp_class_f32_e32 vcc, v8, v1
	s_nop 1
	v_cndmask_b32_e32 v8, v9, v8, vcc
	v_mul_f32_e32 v8, 0x3eb33333, v8
	v_max_f32_e32 v8, 0xda24260, v8
	v_div_scale_f32 v9, s[0:1], v8, v8, 1.0
	v_rcp_f32_e32 v26, v9
	v_div_scale_f32 v27, vcc, 1.0, v8, 1.0
	v_fma_f32 v28, -v9, v26, 1.0
	v_fmac_f32_e32 v26, v28, v26
	v_mul_f32_e32 v28, v27, v26
	v_fma_f32 v29, -v9, v28, v27
	v_fmac_f32_e32 v28, v29, v26
	v_fma_f32 v9, -v9, v28, v27
	v_div_fmas_f32 v9, v9, v26, v28
	v_div_fixup_f32 v9, v9, v8, 1.0
	v_mul_f32_e32 v10, v10, v9
	v_mul_f32_e32 v12, v12, v9
	v_mul_f32_e32 v16, v16, v9
	v_mul_f32_e32 v17, v17, v9
	v_mul_f32_e32 v11, v11, v9
	v_mul_f32_e32 v15, v15, v9
	v_mul_f32_e32 v13, v13, v9
	v_rndne_f32_e32 v10, v10
	v_rndne_f32_e32 v12, v12
	v_rndne_f32_e32 v16, v16
	v_rndne_f32_e32 v17, v17
	v_mul_f32_e32 v14, v14, v9
	v_rndne_f32_e32 v11, v11
	v_rndne_f32_e32 v15, v15
	v_rndne_f32_e32 v13, v13
	v_med3_f32 v10, v10, s13, v4
	v_med3_f32 v12, v12, s13, v4
	v_med3_f32 v16, v16, s13, v4
	v_med3_f32 v17, v17, s13, v4
	v_rndne_f32_e32 v14, v14
	v_med3_f32 v11, v11, s13, v4
	v_med3_f32 v15, v15, s13, v4
	v_med3_f32 v13, v13, s13, v4
	v_cvt_i32_f32_e32 v10, v10
	v_cvt_i32_f32_sdwa v12, v12 dst_sel:WORD_1 dst_unused:UNUSED_PAD src0_sel:DWORD
	v_cvt_i32_f32_e32 v16, v16
	v_cvt_i32_f32_e32 v17, v17
	v_med3_f32 v14, v14, s13, v4
	v_cvt_i32_f32_e32 v11, v11
	v_cvt_i32_f32_e32 v15, v15
	v_cvt_i32_f32_sdwa v13, v13 dst_sel:BYTE_3 dst_unused:UNUSED_PAD src0_sel:DWORD
	v_cvt_i32_f32_e32 v14, v14
	v_and_b32_e32 v10, 15, v10
	v_lshlrev_b32_e32 v16, 20, v16
	v_and_b32_e32 v12, 0xf0000, v12
	v_lshlrev_b32_e32 v17, 28, v17
	v_lshlrev_b32_e32 v15, 12, v15
	v_lshlrev_b32_e32 v11, 8, v11
	v_and_b32_e32 v13, 0xf000000, v13
	v_and_b32_e32 v16, 0xf00000, v16
	v_or3_b32 v10, v10, v17, v12
	v_lshlrev_b32_e32 v14, 4, v14
	v_and_b32_e32 v15, 0xf000, v15
	v_and_b32_e32 v11, 0xf00, v11
	v_or3_b32 v10, v10, v16, v13
	v_and_b32_e32 v14, 0xf0, v14
	v_or3_b32 v10, v10, v11, v15
	v_mul_f32_e32 v18, v18, v9
	v_mul_f32_e32 v22, v22, v9
	v_mul_f32_e32 v19, v19, v9
	v_mul_f32_e32 v23, v23, v9
	v_add_u32_e32 v10, v10, v14
	v_mul_f32_e32 v14, v20, v9
	v_mul_f32_e32 v15, v24, v9
	v_mul_f32_e32 v16, v21, v9
	v_mul_f32_e32 v9, v25, v9
	v_rndne_f32_e32 v18, v18
	v_rndne_f32_e32 v15, v15
	v_rndne_f32_e32 v14, v14
	v_rndne_f32_e32 v9, v9
	v_rndne_f32_e32 v19, v19
	v_rndne_f32_e32 v23, v23
	v_med3_f32 v18, v18, s13, v4
	v_med3_f32 v15, v15, s13, v4
	v_med3_f32 v14, v14, s13, v4
	v_rndne_f32_e32 v16, v16
	v_med3_f32 v9, v9, s13, v4
	v_rndne_f32_e32 v22, v22
	v_med3_f32 v19, v19, s13, v4
	v_med3_f32 v23, v23, s13, v4
	v_cvt_i32_f32_e32 v18, v18
	v_cvt_i32_f32_e32 v15, v15
	v_cvt_i32_f32_sdwa v14, v14 dst_sel:WORD_1 dst_unused:UNUSED_PAD src0_sel:DWORD
	v_med3_f32 v16, v16, s13, v4
	v_cvt_i32_f32_e32 v9, v9
	v_med3_f32 v22, v22, s13, v4
	v_cvt_i32_f32_e32 v23, v23
	v_cvt_i32_f32_e32 v11, v19
	v_cvt_i32_f32_sdwa v16, v16 dst_sel:BYTE_3 dst_unused:UNUSED_PAD src0_sel:DWORD
	v_cvt_i32_f32_e32 v22, v22
	v_and_b32_e32 v18, 15, v18
	v_lshlrev_b32_e32 v15, 20, v15
	v_and_b32_e32 v14, 0xf0000, v14
	v_lshlrev_b32_e32 v9, 28, v9
	v_lshlrev_b32_e32 v13, 12, v23
	v_lshlrev_b32_e32 v11, 8, v11
	v_and_b32_e32 v15, 0xf00000, v15
	v_and_b32_e32 v16, 0xf000000, v16
	v_or3_b32 v9, v18, v9, v14
	v_lshlrev_b32_e32 v22, 4, v22
	v_and_b32_e32 v13, 0xf000, v13
	v_and_b32_e32 v11, 0xf00, v11
	v_or3_b32 v9, v9, v15, v16
	v_and_b32_e32 v12, 0xf0, v22
	v_or3_b32 v9, v9, v11, v13
	v_add_u32_e32 v11, v9, v12
	global_store_dwordx2 v[2:3], v[10:11], off
	s_and_saveexec_b64 s[0:1], s[4:5]
	global_store_dword v5, v8, s[6:7]
	s_or_b64 exec, exec, s[0:1]
	s_add_u32 s6, s6, s20
	s_addc_u32 s7, s7, s21
	v_lshl_add_u64 v[2:3], v[2:3], 0, s[42:43]
	s_branch .Ltabu_loop

; __device__ __forceinline__ unsigned q4(float x) { return (unsigned)(int)fminf(fmaxf(rintf(x), -7.0f), 7.0f) & 0xfu; }
; __device__ __forceinline__ void cvt_table_i4(const float* src, unsigned char* dst, float* scl, float scl_mul, int gw, int ngw, int lane) {
;     for (int row = gw; row < 16384; row += ngw) {
;         const f32x4* sp = (const f32x4*)(src + (size_t)row * 1024 + 16 * lane);
;         const f32x4 a0 = sp[0], a1 = sp[1], a2 = sp[2], a3 = sp[3];
;         float ss = ((a0.x * a0.x + a0.y * a0.y) + (a0.z * a0.z + a0.w * a0.w)) + ((a1.x * a1.x + a1.y * a1.y) + (a1.z * a1.z + a1.w * a1.w))
;                  + ((a2.x * a2.x + a2.y * a2.y) + (a2.z * a2.z + a2.w * a2.w)) + ((a3.x * a3.x + a3.y * a3.y) + (a3.z * a3.z + a3.w * a3.w));
;         ss = wave_sum(ss);
;         const float step = fmaxf(0.35f * sqrtf(ss * (1.0f / 1024.0f)), 1e-30f), q = 1.0f / step;
;         v2u o;
;         o.x = (q4(a0.x * q) | (q4(a1.x * q) << 4)) | ((q4(a0.y * q) | (q4(a1.y * q) << 4)) << 8) | ((q4(a0.z * q) | (q4(a1.z * q) << 4)) << 16) | ((q4(a0.w * q) | (q4(a1.w * q) << 4)) << 24);
;         o.y = (q4(a2.x * q) | (q4(a3.x * q) << 4)) | ((q4(a2.y * q) | (q4(a3.y * q) << 4)) << 8) | ((q4(a2.z * q) | (q4(a3.z * q) << 4)) << 16) | ((q4(a2.w * q) | (q4(a3.w * q) << 4)) << 24);
;         *(v2u*)(dst + (size_t)row * 512 + 8 * lane) = o;
;         if (lane == 0) scl[row] = step * scl_mul;
;     }
.Ltabu_lastA:
	s_waitcnt vmcnt(2)
	v_mul_f32_e32 v8, v11, v11
	v_mul_f32_e32 v9, v13, v13
	v_mul_f32_e32 v26, v15, v15
	v_mul_f32_e32 v27, v17, v17
	v_mul_f32_e32 v28, v19, v19
	v_mul_f32_e32 v29, v21, v21
	v_fmac_f32_e32 v8, v10, v10
	v_fmac_f32_e32 v9, v12, v12
	v_fmac_f32_e32 v26, v14, v14
	v_fmac_f32_e32 v27, v16, v16
	v_mul_f32_e32 v30, v23, v23
	v_mul_f32_e32 v31, v25, v25
	v_fmac_f32_e32 v28, v18, v18
	v_fmac_f32_e32 v29, v20, v20
	v_add_f32_e32 v8, v8, v9
	v_add_f32_e32 v9, v26, v27
	v_fmac_f32_e32 v30, v22, v22
	v_fmac_f32_e32 v31, v24, v24
	v_add_f32_e32 v26, v28, v29
	v_add_f32_e32 v8, v8, v9
	v_add_f32_e32 v27, v30, v31
	v_add_f32_e32 v8, v8, v26
	v_add_f32_e32 v8, v8, v27
	s_nop 1
	v_add_f32_dpp v8, v8, v8 quad_perm:[1,0,3,2] row_mask:0xf bank_mask:0xf bound_ctrl:1
	s_nop 1
	v_add_f32_dpp v8, v8, v8 quad_perm:[2,3,0,1] row_mask:0xf bank_mask:0xf bound_ctrl:1
	s_nop 1
	v_add_f32_dpp v8, v8, v8 row_half_mirror row_mask:0xf bank_mask:0xf bound_ctrl:1
	s_nop 1
	v_add_f32_dpp v8, v8, v8 row_mirror row_mask:0xf bank_mask:0xf bound_ctrl:1
	v_mov_b32_e32 v9, v8
	s_nop 1
	v_permlane16_swap_b32_e32 v8, v9
	v_add_f32 v8, v8, v9
	s_nop 1
	s_nop 0
	v_mov_b32_e32 v9, v8
	s_nop 1
	v_permlane32_swap_b32_e32 v8, v9
	v_add_f32 v8, v8, v9
	s_nop 0
	v_mul_f32_e32 v8, 0x3a800000, v8
	v_mul_f32_e32 v9, 0x4f800000, v8
	v_cmp_gt_f32_e32 vcc, s3, v8
	s_nop 1
	v_cndmask_b32_e32 v8, v8, v9, vcc
	v_sqrt_f32_e32 v9, v8
	s_nop 0
	v_add_u32_e32 v26, -1, v9
	v_add_u32_e32 v27, 1, v9
	v_fma_f32 v28, -v26, v9, v8
	v_fma_f32 v29, -v27, v9, v8
	v_cmp_ge_f32_e64 s[0:1], 0, v28
	s_nop 1
	v_cndmask_b32_e64 v9, v9, v26, s[0:1]
	v_cmp_lt_f32_e64 s[0:1], 0, v29
	s_nop 1
	v_cndmask_b32_e64 v9, v9, v27, s[0:1]
	v_mul_f32_e32 v26, 0x37800000, v9
	v_cndmask_b32_e32 v9, v9, v26, vcc
	v_cmp_class_f32_e32 vcc, v8, v1
	s_nop 1
	v_cndmask_b32_e32 v8, v9, v8, vcc
	v_mul_f32_e32 v8, 0x3eb33333, v8
	v_max_f32_e32 v8, 0xda24260, v8
	v_div_scale_f32 v9, s[0:1], v8, v8, 1.0
	v_rcp_f32_e32 v26, v9
	v_div_scale_f32 v27, vcc, 1.0, v8, 1.0
	v_fma_f32 v28, -v9, v26, 1.0
	v_fmac_f32_e32 v26, v28, v26
	v_mul_f32_e32 v28, v27, v26
	v_fma_f32 v29, -v9, v28, v27
	v_fmac_f32_e32 v28, v29, v26
	v_fma_f32 v9, -v9, v28, v27
	v_div_fmas_f32 v9, v9, v26, v28
	v_div_fixup_f32 v9, v9, v8, 1.0
	v_mul_f32_e32 v10, v10, v9
	v_mul_f32_e32 v12, v12, v9
	v_mul_f32_e32 v16, v16, v9
	v_mul_f32_e32 v17, v17, v9
	v_mul_f32_e32 v11, v11, v9
	v_mul_f32_e32 v15, v15, v9
	v_mul_f32_e32 v13, v13, v9
	v_rndne_f32_e32 v10, v10
	v_rndne_f32_e32 v12, v12
	v_rndne_f32_e32 v16, v16
	v_rndne_f32_e32 v17, v17
	v_mul_f32_e32 v14, v14, v9
	v_rndne_f32_e32 v11, v11
	v_rndne_f32_e32 v15, v15
	v_rndne_f32_e32 v13, v13
	v_med3_f32 v10, v10, s13, v4
	v_med3_f32 v12, v12, s13, v4
	v_med3_f32 v16, v16, s13, v4
	v_med3_f32 v17, v17, s13, v4
	v_rndne_f32_e32 v14, v14
	v_med3_f32 v11, v11, s13, v4
	v_med3_f32 v15, v15, s13, v4
	v_med3_f32 v13, v13, s13, v4
	v_cvt_i32_f32_e32 v10, v10
	v_cvt_i32_f32_sdwa v12, v12 dst_sel:WORD_1 dst_unused:UNUSED_PAD src0_sel:DWORD
	v_cvt_i32_f32_e32 v16, v16
	v_cvt_i32_f32_e32 v17, v17
	v_med3_f32 v14, v14, s13, v4
	v_cvt_i32_f32_e32 v11, v11
	v_cvt_i32_f32_e32 v15, v15
	v_cvt_i32_f32_sdwa v13, v13 dst_sel:BYTE_3 dst_unused:UNUSED_PAD src0_sel:DWORD
	v_cvt_i32_f32_e32 v14, v14
	v_and_b32_e32 v10, 15, v10
	v_lshlrev_b32_e32 v16, 20, v16
	v_and_b32_e32 v12, 0xf0000, v12
	v_lshlrev_b32_e32 v17, 28, v17
	v_lshlrev_b32_e32 v15, 12, v15
	v_lshlrev_b32_e32 v11, 8, v11
	v_and_b32_e32 v13, 0xf000000, v13
	v_and_b32_e32 v16, 0xf00000, v16
	v_or3_b32 v10, v10, v17, v12
	v_lshlrev_b32_e32 v14, 4, v14
	v_and_b32_e32 v15, 0xf000, v15
	v_and_b32_e32 v11, 0xf00, v11
	v_or3_b32 v10, v10, v16, v13
	v_and_b32_e32 v14, 0xf0, v14
	v_or3_b32 v10, v10, v11, v15
	v_mul_f32_e32 v18, v18, v9
	v_mul_f32_e32 v22, v22, v9
	v_mul_f32_e32 v19, v19, v9
	v_mul_f32_e32 v23, v23, v9
	v_add_u32_e32 v10, v10, v14
	v_mul_f32_e32 v14, v20, v9
	v_mul_f32_e32 v15, v24, v9
	v_mul_f32_e32 v16, v21, v9
	v_mul_f32_e32 v9, v25, v9
	v_rndne_f32_e32 v18, v18
	v_rndne_f32_e32 v15, v15
	v_rndne_f32_e32 v14, v14
	v_rndne_f32_e32 v9, v9
	v_rndne_f32_e32 v19, v19
	v_rndne_f32_e32 v23, v23
	v_med3_f32 v18, v18, s13, v4
	v_med3_f32 v15, v15, s13, v4
	v_med3_f32 v14, v14, s13, v4
	v_rndne_f32_e32 v16, v16
	v_med3_f32 v9, v9, s13, v4
	v_rndne_f32_e32 v22, v22
	v_med3_f32 v19, v19, s13, v4
	v_med3_f32 v23, v23, s13, v4
	v_cvt_i32_f32_e32 v18, v18
	v_cvt_i32_f32_e32 v15, v15
	v_cvt_i32_f32_sdwa v14, v14 dst_sel:WORD_1 dst_unused:UNUSED_PAD src0_sel:DWORD
	v_med3_f32 v16, v16, s13, v4
	v_cvt_i32_f32_e32 v9, v9
	v_med3_f32 v22, v22, s13, v4
	v_cvt_i32_f32_e32 v23, v23
	v_cvt_i32_f32_e32 v11, v19
	v_cvt_i32_f32_sdwa v16, v16 dst_sel:BYTE_3 dst_unused:UNUSED_PAD src0_sel:DWORD
	v_cvt_i32_f32_e32 v22, v22
	v_and_b32_e32 v18, 15, v18
	v_lshlrev_b32_e32 v15, 20, v15
	v_and_b32_e32 v14, 0xf0000, v14
	v_lshlrev_b32_e32 v9, 28, v9
	v_lshlrev_b32_e32 v13, 12, v23
	v_lshlrev_b32_e32 v11, 8, v11
	v_and_b32_e32 v15, 0xf00000, v15
	v_and_b32_e32 v16, 0xf000000, v16
	v_or3_b32 v9, v18, v9, v14
	v_lshlrev_b32_e32 v22, 4, v22
	v_and_b32_e32 v13, 0xf000, v13
	v_and_b32_e32 v11, 0xf00, v11
	v_or3_b32 v9, v9, v15, v16
	v_and_b32_e32 v12, 0xf0, v22
	v_or3_b32 v9, v9, v11, v13
	v_add_u32_e32 v11, v9, v12
	global_store_dwordx2 v[2:3], v[10:11], off
	s_and_saveexec_b64 s[0:1], s[4:5]
	global_store_dword v5, v8, s[6:7]
	s_or_b64 exec, exec, s[0:1]
	s_branch .LBB0_2027
; __device__ __forceinline__ unsigned q4(float x) { return (unsigned)(int)fminf(fmaxf(rintf(x), -7.0f), 7.0f) & 0xfu; }
; __device__ __forceinline__ void cvt_table_i4(const float* src, unsigned char* dst, float* scl, float scl_mul, int gw, int ngw, int lane) {
;     for (int row = gw; row < 16384; row += ngw) {
;         const f32x4* sp = (const f32x4*)(src + (size_t)row * 1024 + 16 * lane);
;         const f32x4 a0 = sp[0], a1 = sp[1], a2 = sp[2], a3 = sp[3];
;         float ss = ((a0.x * a0.x + a0.y * a0.y) + (a0.z * a0.z + a0.w * a0.w)) + ((a1.x * a1.x + a1.y * a1.y) + (a1.z * a1.z + a1.w * a1.w))
;                  + ((a2.x * a2.x + a2.y * a2.y) + (a2.z * a2.z + a2.w * a2.w)) + ((a3.x * a3.x + a3.y * a3.y) + (a3.z * a3.z + a3.w * a3.w));
;         ss = wave_sum(ss);
;         const float step = fmaxf(0.35f * sqrtf(ss * (1.0f / 1024.0f)), 1e-30f), q = 1.0f / step;
;         v2u o;
;         o.x = (q4(a0.x * q) | (q4(a1.x * q) << 4)) | ((q4(a0.y * q) | (q4(a1.y * q) << 4)) << 8) | ((q4(a0.z * q) | (q4(a1.z * q) << 4)) << 16) | ((q4(a0.w * q) | (q4(a1.w * q) << 4)) << 24);
;         o.y = (q4(a2.x * q) | (q4(a3.x * q) << 4)) | ((q4(a2.y * q) | (q4(a3.y * q) << 4)) << 8) | ((q4(a2.z * q) | (q4(a3.z * q) << 4)) << 16) | ((q4(a2.w * q) | (q4(a3.w * q) << 4)) << 24);
;         *(v2u*)(dst + (size_t)row * 512 + 8 * lane) = o;
;         if (lane == 0) scl[row] = step * scl_mul;
;     }
.Ltabu_lastB:
	s_waitcnt vmcnt(2)
	v_mul_f32_e32 v48, v51, v51
	v_mul_f32_e32 v49, v53, v53
	v_mul_f32_e32 v66, v55, v55
	v_mul_f32_e32 v67, v57, v57
	v_mul_f32_e32 v68, v59, v59
	v_mul_f32_e32 v69, v61, v61
	v_fmac_f32_e32 v48, v50, v50
	v_fmac_f32_e32 v49, v52, v52
	v_fmac_f32_e32 v66, v54, v54
	v_fmac_f32_e32 v67, v56, v56
	v_mul_f32_e32 v70, v63, v63
	v_mul_f32_e32 v71, v65, v65
	v_fmac_f32_e32 v68, v58, v58
	v_fmac_f32_e32 v69, v60, v60
	v_add_f32_e32 v48, v48, v49
	v_add_f32_e32 v49, v66, v67
	v_fmac_f32_e32 v70, v62, v62
	v_fmac_f32_e32 v71, v64, v64
	v_add_f32_e32 v66, v68, v69
	v_add_f32_e32 v48, v48, v49
	v_add_f32_e32 v67, v70, v71
	v_add_f32_e32 v48, v48, v66
	v_add_f32_e32 v48, v48, v67
	s_nop 1
	v_add_f32_dpp v48, v48, v48 quad_perm:[1,0,3,2] row_mask:0xf bank_mask:0xf bound_ctrl:1
	s_nop 1
	v_add_f32_dpp v48, v48, v48 quad_perm:[2,3,0,1] row_mask:0xf bank_mask:0xf bound_ctrl:1
	s_nop 1
	v_add_f32_dpp v48, v48, v48 row_half_mirror row_mask:0xf bank_mask:0xf bound_ctrl:1
	s_nop 1
	v_add_f32_dpp v48, v48, v48 row_mirror row_mask:0xf bank_mask:0xf bound_ctrl:1
	v_mov_b32_e32 v49, v48
	s_nop 1
	v_permlane16_swap_b32_e32 v48, v49
	v_add_f32 v48, v48, v49
	s_nop 1
	s_nop 0
	v_mov_b32_e32 v49, v48
	s_nop 1
	v_permlane32_swap_b32_e32 v48, v49
	v_add_f32 v48, v48, v49
	s_nop 0
	v_mul_f32_e32 v48, 0x3a800000, v48
	v_mul_f32_e32 v49, 0x4f800000, v48
	v_cmp_gt_f32_e32 vcc, s3, v48
	s_nop 1
	v_cndmask_b32_e32 v48, v48, v49, vcc
	v_sqrt_f32_e32 v49, v48
	s_nop 0
	v_add_u32_e32 v66, -1, v49
	v_add_u32_e32 v67, 1, v49
	v_fma_f32 v68, -v66, v49, v48
	v_fma_f32 v69, -v67, v49, v48
	v_cmp_ge_f32_e64 s[0:1], 0, v68
	s_nop 1
	v_cndmask_b32_e64 v49, v49, v66, s[0:1]
	v_cmp_lt_f32_e64 s[0:1], 0, v69
	s_nop 1
	v_cndmask_b32_e64 v49, v49, v67, s[0:1]
	v_mul_f32_e32 v66, 0x37800000, v49
	v_cndmask_b32_e32 v49, v49, v66, vcc
	v_cmp_class_f32_e32 vcc, v48, v1
	s_nop 1
	v_cndmask_b32_e32 v48, v49, v48, vcc
	v_mul_f32_e32 v48, 0x3eb33333, v48
	v_max_f32_e32 v48, 0xda24260, v48
	v_div_scale_f32 v49, s[0:1], v48, v48, 1.0
	v_rcp_f32_e32 v66, v49
	v_div_scale_f32 v67, vcc, 1.0, v48, 1.0
	v_fma_f32 v68, -v49, v66, 1.0
	v_fmac_f32_e32 v66, v68, v66
	v_mul_f32_e32 v68, v67, v66
	v_fma_f32 v69, -v49, v68, v67
	v_fmac_f32_e32 v68, v69, v66
	v_fma_f32 v49, -v49, v68, v67
	v_div_fmas_f32 v49, v49, v66, v68
	v_div_fixup_f32 v49, v49, v48, 1.0
	v_mul_f32_e32 v50, v50, v49
	v_mul_f32_e32 v52, v52, v49
	v_mul_f32_e32 v56, v56, v49
	v_mul_f32_e32 v57, v57, v49
	v_mul_f32_e32 v51, v51, v49
	v_mul_f32_e32 v55, v55, v49
	v_mul_f32_e32 v53, v53, v49
	v_rndne_f32_e32 v50, v50
	v_rndne_f32_e32 v52, v52
	v_rndne_f32_e32 v56, v56
	v_rndne_f32_e32 v57, v57
	v_mul_f32_e32 v54, v54, v49
	v_rndne_f32_e32 v51, v51
	v_rndne_f32_e32 v55, v55
	v_rndne_f32_e32 v53, v53
	v_med3_f32 v50, v50, s13, v4
	v_med3_f32 v52, v52, s13, v4
	v_med3_f32 v56, v56, s13, v4
	v_med3_f32 v57, v57, s13, v4
	v_rndne_f32_e32 v54, v54
	v_med3_f32 v51, v51, s13, v4
	v_med3_f32 v55, v55, s13, v4
	v_med3_f32 v53, v53, s13, v4
	v_cvt_i32_f32_e32 v50, v50
	v_cvt_i32_f32_sdwa v52, v52 dst_sel:WORD_1 dst_unused:UNUSED_PAD src0_sel:DWORD
	v_cvt_i32_f32_e32 v56, v56
	v_cvt_i32_f32_e32 v57, v57
	v_med3_f32 v54, v54, s13, v4
	v_cvt_i32_f32_e32 v51, v51
	v_cvt_i32_f32_e32 v55, v55
	v_cvt_i32_f32_sdwa v53, v53 dst_sel:BYTE_3 dst_unused:UNUSED_PAD src0_sel:DWORD
	v_cvt_i32_f32_e32 v54, v54
	v_and_b32_e32 v50, 15, v50
	v_lshlrev_b32_e32 v56, 20, v56
	v_and_b32_e32 v52, 0xf0000, v52
	v_lshlrev_b32_e32 v57, 28, v57
	v_lshlrev_b32_e32 v55, 12, v55
	v_lshlrev_b32_e32 v51, 8, v51
	v_and_b32_e32 v53, 0xf000000, v53
	v_and_b32_e32 v56, 0xf00000, v56
	v_or3_b32 v50, v50, v57, v52
	v_lshlrev_b32_e32 v54, 4, v54
	v_and_b32_e32 v55, 0xf000, v55
	v_and_b32_e32 v51, 0xf00, v51
	v_or3_b32 v50, v50, v56, v53
	v_and_b32_e32 v54, 0xf0, v54
	v_or3_b32 v50, v50, v51, v55
	v_mul_f32_e32 v58, v58, v49
	v_mul_f32_e32 v62, v62, v49
	v_mul_f32_e32 v59, v59, v49
	v_mul_f32_e32 v63, v63, v49
	v_add_u32_e32 v50, v50, v54
	v_mul_f32_e32 v54, v60, v49
	v_mul_f32_e32 v55, v64, v49
	v_mul_f32_e32 v56, v61, v49
	v_mul_f32_e32 v49, v65, v49
	v_rndne_f32_e32 v58, v58
	v_rndne_f32_e32 v55, v55
	v_rndne_f32_e32 v54, v54
	v_rndne_f32_e32 v49, v49
	v_rndne_f32_e32 v59, v59
	v_rndne_f32_e32 v63, v63
	v_med3_f32 v58, v58, s13, v4
	v_med3_f32 v55, v55, s13, v4
	v_med3_f32 v54, v54, s13, v4
	v_rndne_f32_e32 v56, v56
	v_med3_f32 v49, v49, s13, v4
	v_rndne_f32_e32 v62, v62
	v_med3_f32 v59, v59, s13, v4
	v_med3_f32 v63, v63, s13, v4
	v_cvt_i32_f32_e32 v58, v58
	v_cvt_i32_f32_e32 v55, v55
	v_cvt_i32_f32_sdwa v54, v54 dst_sel:WORD_1 dst_unused:UNUSED_PAD src0_sel:DWORD
	v_med3_f32 v56, v56, s13, v4
	v_cvt_i32_f32_e32 v49, v49
	v_med3_f32 v62, v62, s13, v4
	v_cvt_i32_f32_e32 v63, v63
	v_cvt_i32_f32_e32 v51, v59
	v_cvt_i32_f32_sdwa v56, v56 dst_sel:BYTE_3 dst_unused:UNUSED_PAD src0_sel:DWORD
	v_cvt_i32_f32_e32 v62, v62
	v_and_b32_e32 v58, 15, v58
	v_lshlrev_b32_e32 v55, 20, v55
	v_and_b32_e32 v54, 0xf0000, v54
	v_lshlrev_b32_e32 v49, 28, v49
	v_lshlrev_b32_e32 v53, 12, v63
	v_lshlrev_b32_e32 v51, 8, v51
	v_and_b32_e32 v55, 0xf00000, v55
	v_and_b32_e32 v56, 0xf000000, v56
	v_or3_b32 v49, v58, v49, v54
	v_lshlrev_b32_e32 v62, 4, v62
	v_and_b32_e32 v53, 0xf000, v53
	v_and_b32_e32 v51, 0xf00, v51
	v_or3_b32 v49, v49, v55, v56
	v_and_b32_e32 v52, 0xf0, v62
	v_or3_b32 v49, v49, v51, v53
	v_add_u32_e32 v51, v49, v52
	global_store_dwordx2 v[2:3], v[50:51], off
	s_and_saveexec_b64 s[0:1], s[4:5]
	global_store_dword v5, v48, s[6:7]
	s_or_b64 exec, exec, s[0:1]
